# v046 + leading wave half (wr==0) runs its GEMM epilogue at s_setprio 3 so its next-tile decode and first load segment hide under the trailing half's epilogue; priority reset behind the epilogue
# speedup vs baseline: 1.0096x; 1.0067x over previous
.LBB0_253:
	s_setprio 0
	s_andn2_b64 vcc, exec, s[0:1]
	s_mov_b32 s2, s56
	s_mov_b32 s74, s68
	s_mov_b64 s[80:81], s[72:73]
	s_mov_b64 s[82:83], s[70:71]
	s_cbranch_vccz .LBB0_271

.LBB0_261:
	ds_read_b128 v[144:147], v170
	ds_read_b128 v[148:151], v170 offset:1024
	ds_read_b128 v[174:177], v170 offset:2048
	ds_read_b128 v[178:181], v170 offset:3072
	ds_read_b128 v[182:185], v171
	ds_read_b128 v[186:189], v171 offset:1024
	ds_read_b128 v[190:193], v171 offset:2048
	ds_read_b128 v[194:197], v171 offset:3072
	s_add_u32 s26, s80, 0xfff80080
	s_addc_u32 s27, s81, -1
	s_cmp_eq_u32 vcc_hi, 28
	s_cselect_b32 s83, s69, s27
	s_cselect_b32 s82, s75, s26
	s_cselect_b32 s27, s57, vcc_lo
	s_cselect_b32 s26, s96, s97
	v_lshl_add_u64 v[152:153], s[80:81], 0, v[134:135]
	s_add_i32 m0, s87, 0xc000
	ds_read_b128 v[198:201], v172
	ds_read_b128 v[202:205], v172 offset:1024
	ds_read_b128 v[206:209], v172 offset:2048
	ds_read_b128 v[210:213], v172 offset:3072
	ds_read_b128 v[214:217], v172 offset:4096
	ds_read_b128 v[220:223], v172 offset:5120
	ds_read_b128 v[224:227], v172 offset:6144
	ds_read_b128 v[228:231], v172 offset:7168
	global_load_lds_dwordx4 v[152:153], off
	v_lshl_add_u64 v[152:153], s[80:81], 0, v[138:139]
	s_add_i32 m0, s87, 0xe000
	s_nop 0
	global_load_lds_dwordx4 v[152:153], off
	s_waitcnt vmcnt(8)
	s_waitcnt lgkmcnt(0)
	s_barrier
	v_mfma_f32_16x16x32_bf16 v[122:125], v[144:147], v[198:201], v[122:125]
	v_mfma_f32_16x16x32_bf16 v[118:121], v[174:177], v[198:201], v[118:121]
	v_mfma_f32_16x16x32_bf16 v[106:109], v[144:147], v[206:209], v[106:109]
	v_mfma_f32_16x16x32_bf16 v[102:105], v[174:177], v[206:209], v[102:105]
	v_mfma_f32_16x16x32_bf16 v[90:93], v[144:147], v[214:217], v[90:93]
	v_mfma_f32_16x16x32_bf16 v[86:89], v[174:177], v[214:217], v[86:89]
	v_mfma_f32_16x16x32_bf16 v[74:77], v[144:147], v[224:227], v[74:77]
	v_mfma_f32_16x16x32_bf16 v[70:73], v[174:177], v[224:227], v[70:73]
	v_mfma_f32_16x16x32_bf16 v[122:125], v[148:151], v[202:205], v[122:125]
	v_mfma_f32_16x16x32_bf16 v[118:121], v[178:181], v[202:205], v[118:121]
	v_mfma_f32_16x16x32_bf16 v[106:109], v[148:151], v[210:213], v[106:109]
	v_mfma_f32_16x16x32_bf16 v[102:105], v[178:181], v[210:213], v[102:105]
	v_mfma_f32_16x16x32_bf16 v[90:93], v[148:151], v[220:223], v[90:93]
	v_mfma_f32_16x16x32_bf16 v[86:89], v[178:181], v[220:223], v[86:89]
	v_mfma_f32_16x16x32_bf16 v[74:77], v[148:151], v[228:231], v[74:77]
	v_mfma_f32_16x16x32_bf16 v[70:73], v[178:181], v[228:231], v[70:73]
	v_mfma_f32_16x16x32_bf16 v[126:129], v[182:185], v[198:201], v[126:129]
	v_mfma_f32_16x16x32_bf16 v[114:117], v[190:193], v[198:201], v[114:117]
	v_mfma_f32_16x16x32_bf16 v[110:113], v[182:185], v[206:209], v[110:113]
	v_mfma_f32_16x16x32_bf16 v[98:101], v[190:193], v[206:209], v[98:101]
	v_mfma_f32_16x16x32_bf16 v[94:97], v[182:185], v[214:217], v[94:97]
	v_mfma_f32_16x16x32_bf16 v[82:85], v[190:193], v[214:217], v[82:85]
	v_mfma_f32_16x16x32_bf16 v[78:81], v[182:185], v[224:227], v[78:81]
	v_mfma_f32_16x16x32_bf16 v[66:69], v[190:193], v[224:227], v[66:69]
	v_mfma_f32_16x16x32_bf16 v[126:129], v[186:189], v[202:205], v[126:129]
	v_mfma_f32_16x16x32_bf16 v[114:117], v[194:197], v[202:205], v[114:117]
	v_mfma_f32_16x16x32_bf16 v[110:113], v[186:189], v[210:213], v[110:113]
	v_mfma_f32_16x16x32_bf16 v[98:101], v[194:197], v[210:213], v[98:101]
	v_mfma_f32_16x16x32_bf16 v[94:97], v[186:189], v[220:223], v[94:97]
	v_mfma_f32_16x16x32_bf16 v[82:85], v[194:197], v[220:223], v[82:85]
	v_mfma_f32_16x16x32_bf16 v[78:81], v[186:189], v[228:231], v[78:81]
	v_mfma_f32_16x16x32_bf16 v[66:69], v[194:197], v[228:231], v[66:69]
	s_barrier
	v_lshl_add_u64 v[152:153], s[26:27], 0, v[162:163]
	s_add_i32 s26, s94, s86
	s_mov_b32 m0, s26
	ds_read_b128 v[198:201], v172 offset:16384
	ds_read_b128 v[202:205], v172 offset:17408
	ds_read_b128 v[206:209], v172 offset:18432
	ds_read_b128 v[210:213], v172 offset:19456
	ds_read_b128 v[214:217], v172 offset:20480
	ds_read_b128 v[220:223], v172 offset:21504
	ds_read_b128 v[224:227], v172 offset:22528
	ds_read_b128 v[228:231], v172 offset:23552
	global_load_lds_dwordx4 v[152:153], off
	v_lshl_add_u64 v[232:233], v[152:153], 0, s[10:11]
	s_add_i32 m0, s26, 0x2000
	s_add_i32 s26, s95, s86
	global_load_lds_dwordx4 v[232:233], off
	v_lshl_add_u64 v[232:233], v[152:153], 0, s[12:13]
	s_mov_b32 m0, s26
	v_lshl_add_u64 v[234:235], s[82:83], 0, v[132:133]
	global_load_lds_dwordx4 v[232:233], off
	v_lshl_add_u64 v[232:233], v[152:153], 0, s[14:15]
	s_add_i32 m0, s26, 0x2000
	s_nop 0
	global_load_lds_dwordx4 v[232:233], off
	v_lshl_add_u64 v[232:233], s[82:83], 0, v[130:131]
	s_mov_b32 m0, s87
	s_nop 0
	global_load_lds_dwordx4 v[232:233], off
	s_mov_b32 m0, s88
	s_nop 0
	global_load_lds_dwordx4 v[234:235], off
	s_waitcnt vmcnt(8)
	s_waitcnt lgkmcnt(0)
	s_barrier
	v_mfma_f32_16x16x32_bf16 v[58:61], v[144:147], v[198:201], v[58:61]
	v_mfma_f32_16x16x32_bf16 v[54:57], v[174:177], v[198:201], v[54:57]
	v_mfma_f32_16x16x32_bf16 v[42:45], v[144:147], v[206:209], v[42:45]
	v_mfma_f32_16x16x32_bf16 v[38:41], v[174:177], v[206:209], v[38:41]
	v_mfma_f32_16x16x32_bf16 v[26:29], v[144:147], v[214:217], v[26:29]
	v_mfma_f32_16x16x32_bf16 v[22:25], v[174:177], v[214:217], v[22:25]
	v_mfma_f32_16x16x32_bf16 v[10:13], v[144:147], v[224:227], v[10:13]
	v_mfma_f32_16x16x32_bf16 v[6:9], v[174:177], v[224:227], v[6:9]
	v_mfma_f32_16x16x32_bf16 v[58:61], v[148:151], v[202:205], v[58:61]
	v_mfma_f32_16x16x32_bf16 v[54:57], v[178:181], v[202:205], v[54:57]
	v_mfma_f32_16x16x32_bf16 v[42:45], v[148:151], v[210:213], v[42:45]
	v_mfma_f32_16x16x32_bf16 v[38:41], v[178:181], v[210:213], v[38:41]
	v_mfma_f32_16x16x32_bf16 v[26:29], v[148:151], v[220:223], v[26:29]
	v_mfma_f32_16x16x32_bf16 v[22:25], v[178:181], v[220:223], v[22:25]
	v_mfma_f32_16x16x32_bf16 v[10:13], v[148:151], v[228:231], v[10:13]
	v_mfma_f32_16x16x32_bf16 v[6:9], v[178:181], v[228:231], v[6:9]
	v_mfma_f32_16x16x32_bf16 v[62:65], v[182:185], v[198:201], v[62:65]
	v_mfma_f32_16x16x32_bf16 v[50:53], v[190:193], v[198:201], v[50:53]
	v_mfma_f32_16x16x32_bf16 v[46:49], v[182:185], v[206:209], v[46:49]
	v_mfma_f32_16x16x32_bf16 v[34:37], v[190:193], v[206:209], v[34:37]
	v_mfma_f32_16x16x32_bf16 v[30:33], v[182:185], v[214:217], v[30:33]
	v_mfma_f32_16x16x32_bf16 v[18:21], v[190:193], v[214:217], v[18:21]
	v_mfma_f32_16x16x32_bf16 v[14:17], v[182:185], v[224:227], v[14:17]
	v_mfma_f32_16x16x32_bf16 v[2:5], v[190:193], v[224:227], v[2:5]
	v_mfma_f32_16x16x32_bf16 v[62:65], v[186:189], v[202:205], v[62:65]
	v_mfma_f32_16x16x32_bf16 v[50:53], v[194:197], v[202:205], v[50:53]
	v_mfma_f32_16x16x32_bf16 v[46:49], v[186:189], v[210:213], v[46:49]
	v_mfma_f32_16x16x32_bf16 v[34:37], v[194:197], v[210:213], v[34:37]
	v_mfma_f32_16x16x32_bf16 v[30:33], v[186:189], v[220:223], v[30:33]
	v_mfma_f32_16x16x32_bf16 v[18:21], v[194:197], v[220:223], v[18:21]
	v_mfma_f32_16x16x32_bf16 v[14:17], v[186:189], v[228:231], v[14:17]
	v_mfma_f32_16x16x32_bf16 v[2:5], v[194:197], v[228:231], v[2:5]
	s_barrier
	s_add_i32 s33, 0, 0x18000
	v_add_u32_e32 v136, s33, v167
	s_add_i32 s8, 0, 0x1c000
	ds_read_b128 v[144:147], v136
	ds_read_b128 v[148:151], v136 offset:1024
	ds_read_b128 v[174:177], v136 offset:2048
	ds_read_b128 v[178:181], v136 offset:3072
	v_add_u32_e32 v136, s8, v167
	ds_read_b128 v[182:185], v136
	ds_read_b128 v[186:189], v136 offset:1024
	ds_read_b128 v[190:193], v136 offset:2048
	ds_read_b128 v[194:197], v136 offset:3072
	s_add_u32 s26, s82, 0x80000
	s_addc_u32 s27, s83, 0
	s_mov_b32 m0, s89
	v_lshl_add_u64 v[236:237], s[26:27], 0, v[130:131]
	ds_read_b128 v[198:201], v172 offset:32768
	ds_read_b128 v[202:205], v172 offset:33792
	ds_read_b128 v[206:209], v172 offset:34816
	ds_read_b128 v[210:213], v172 offset:35840
	ds_read_b128 v[214:217], v172 offset:36864
	ds_read_b128 v[220:223], v172 offset:37888
	ds_read_b128 v[224:227], v172 offset:38912
	ds_read_b128 v[228:231], v172 offset:39936
	global_load_lds_dwordx4 v[236:237], off
	v_lshl_add_u64 v[236:237], s[26:27], 0, v[132:133]
	s_mov_b32 m0, s90
	s_nop 0
	global_load_lds_dwordx4 v[236:237], off
	s_waitcnt vmcnt(8)
	s_waitcnt lgkmcnt(0)
	s_barrier
	v_mfma_f32_16x16x32_bf16 v[122:125], v[144:147], v[198:201], v[122:125]
	v_mfma_f32_16x16x32_bf16 v[118:121], v[174:177], v[198:201], v[118:121]
	v_mfma_f32_16x16x32_bf16 v[106:109], v[144:147], v[206:209], v[106:109]
	v_mfma_f32_16x16x32_bf16 v[102:105], v[174:177], v[206:209], v[102:105]
	v_mfma_f32_16x16x32_bf16 v[90:93], v[144:147], v[214:217], v[90:93]
	v_mfma_f32_16x16x32_bf16 v[86:89], v[174:177], v[214:217], v[86:89]
	v_mfma_f32_16x16x32_bf16 v[74:77], v[144:147], v[224:227], v[74:77]
	v_mfma_f32_16x16x32_bf16 v[70:73], v[174:177], v[224:227], v[70:73]
	v_mfma_f32_16x16x32_bf16 v[122:125], v[148:151], v[202:205], v[122:125]
	v_mfma_f32_16x16x32_bf16 v[118:121], v[178:181], v[202:205], v[118:121]
	v_mfma_f32_16x16x32_bf16 v[106:109], v[148:151], v[210:213], v[106:109]
	v_mfma_f32_16x16x32_bf16 v[102:105], v[178:181], v[210:213], v[102:105]
	v_mfma_f32_16x16x32_bf16 v[90:93], v[148:151], v[220:223], v[90:93]
	v_mfma_f32_16x16x32_bf16 v[86:89], v[178:181], v[220:223], v[86:89]
	v_mfma_f32_16x16x32_bf16 v[74:77], v[148:151], v[228:231], v[74:77]
	v_mfma_f32_16x16x32_bf16 v[70:73], v[178:181], v[228:231], v[70:73]
	v_mfma_f32_16x16x32_bf16 v[126:129], v[182:185], v[198:201], v[126:129]
	v_mfma_f32_16x16x32_bf16 v[114:117], v[190:193], v[198:201], v[114:117]
	v_mfma_f32_16x16x32_bf16 v[110:113], v[182:185], v[206:209], v[110:113]
	v_mfma_f32_16x16x32_bf16 v[98:101], v[190:193], v[206:209], v[98:101]
	v_mfma_f32_16x16x32_bf16 v[94:97], v[182:185], v[214:217], v[94:97]
	v_mfma_f32_16x16x32_bf16 v[82:85], v[190:193], v[214:217], v[82:85]
	v_mfma_f32_16x16x32_bf16 v[78:81], v[182:185], v[224:227], v[78:81]
	v_mfma_f32_16x16x32_bf16 v[66:69], v[190:193], v[224:227], v[66:69]
	v_mfma_f32_16x16x32_bf16 v[126:129], v[186:189], v[202:205], v[126:129]
	v_mfma_f32_16x16x32_bf16 v[114:117], v[194:197], v[202:205], v[114:117]
	v_mfma_f32_16x16x32_bf16 v[110:113], v[186:189], v[210:213], v[110:113]
	v_mfma_f32_16x16x32_bf16 v[98:101], v[194:197], v[210:213], v[98:101]
	v_mfma_f32_16x16x32_bf16 v[94:97], v[186:189], v[220:223], v[94:97]
	v_mfma_f32_16x16x32_bf16 v[82:85], v[194:197], v[220:223], v[82:85]
	v_mfma_f32_16x16x32_bf16 v[78:81], v[186:189], v[228:231], v[78:81]
	v_mfma_f32_16x16x32_bf16 v[66:69], v[194:197], v[228:231], v[66:69]
	s_barrier
	s_add_i32 s9, s33, s86
	v_lshl_add_u64 v[236:237], v[152:153], 0, s[20:21]
	s_mov_b32 m0, s9
	ds_read_b128 v[198:201], v172 offset:49152
	ds_read_b128 v[202:205], v172 offset:50176
	ds_read_b128 v[206:209], v172 offset:51200
	ds_read_b128 v[210:213], v172 offset:52224
	ds_read_b128 v[214:217], v172 offset:53248
	ds_read_b128 v[220:223], v172 offset:54272
	ds_read_b128 v[224:227], v172 offset:55296
	ds_read_b128 v[228:231], v172 offset:56320
	global_load_lds_dwordx4 v[236:237], off
	v_lshl_add_u64 v[236:237], v[152:153], 0, s[22:23]
	s_add_i32 m0, s9, 0x2000
	s_add_i32 s8, s8, s86
	global_load_lds_dwordx4 v[236:237], off
	v_lshl_add_u64 v[236:237], v[152:153], 0, s[40:41]
	s_mov_b32 m0, s8
	v_lshl_add_u64 v[152:153], v[152:153], 0, s[44:45]
	global_load_lds_dwordx4 v[236:237], off
	s_add_i32 m0, s8, 0x2000
	s_nop 0
	global_load_lds_dwordx4 v[152:153], off
	v_lshl_add_u64 v[152:153], v[232:233], 0, s[24:25]
	s_mov_b32 m0, s91
	s_nop 0
	global_load_lds_dwordx4 v[152:153], off
	v_lshl_add_u64 v[152:153], v[234:235], 0, s[24:25]
	s_mov_b32 m0, s92
	s_nop 0
	global_load_lds_dwordx4 v[152:153], off
	s_waitcnt vmcnt(8)
	s_waitcnt lgkmcnt(0)
	s_barrier
	v_mfma_f32_16x16x32_bf16 v[58:61], v[144:147], v[198:201], v[58:61]
	v_mfma_f32_16x16x32_bf16 v[54:57], v[174:177], v[198:201], v[54:57]
	v_mfma_f32_16x16x32_bf16 v[42:45], v[144:147], v[206:209], v[42:45]
	v_mfma_f32_16x16x32_bf16 v[38:41], v[174:177], v[206:209], v[38:41]
	v_mfma_f32_16x16x32_bf16 v[26:29], v[144:147], v[214:217], v[26:29]
	v_mfma_f32_16x16x32_bf16 v[22:25], v[174:177], v[214:217], v[22:25]
	v_mfma_f32_16x16x32_bf16 v[10:13], v[144:147], v[224:227], v[10:13]
	v_mfma_f32_16x16x32_bf16 v[6:9], v[174:177], v[224:227], v[6:9]
	v_mfma_f32_16x16x32_bf16 v[58:61], v[148:151], v[202:205], v[58:61]
	v_mfma_f32_16x16x32_bf16 v[54:57], v[178:181], v[202:205], v[54:57]
	v_mfma_f32_16x16x32_bf16 v[42:45], v[148:151], v[210:213], v[42:45]
	v_mfma_f32_16x16x32_bf16 v[38:41], v[178:181], v[210:213], v[38:41]
	v_mfma_f32_16x16x32_bf16 v[26:29], v[148:151], v[220:223], v[26:29]
	v_mfma_f32_16x16x32_bf16 v[22:25], v[178:181], v[220:223], v[22:25]
	v_mfma_f32_16x16x32_bf16 v[10:13], v[148:151], v[228:231], v[10:13]
	v_mfma_f32_16x16x32_bf16 v[6:9], v[178:181], v[228:231], v[6:9]
	v_mfma_f32_16x16x32_bf16 v[62:65], v[182:185], v[198:201], v[62:65]
	v_mfma_f32_16x16x32_bf16 v[50:53], v[190:193], v[198:201], v[50:53]
	v_mfma_f32_16x16x32_bf16 v[46:49], v[182:185], v[206:209], v[46:49]
	v_mfma_f32_16x16x32_bf16 v[34:37], v[190:193], v[206:209], v[34:37]
	v_mfma_f32_16x16x32_bf16 v[30:33], v[182:185], v[214:217], v[30:33]
	v_mfma_f32_16x16x32_bf16 v[18:21], v[190:193], v[214:217], v[18:21]
	v_mfma_f32_16x16x32_bf16 v[14:17], v[182:185], v[224:227], v[14:17]
	v_mfma_f32_16x16x32_bf16 v[2:5], v[190:193], v[224:227], v[2:5]
	v_mfma_f32_16x16x32_bf16 v[62:65], v[186:189], v[202:205], v[62:65]
	v_mfma_f32_16x16x32_bf16 v[50:53], v[194:197], v[202:205], v[50:53]
	v_mfma_f32_16x16x32_bf16 v[46:49], v[186:189], v[210:213], v[46:49]
	v_mfma_f32_16x16x32_bf16 v[34:37], v[194:197], v[210:213], v[34:37]
	v_mfma_f32_16x16x32_bf16 v[30:33], v[186:189], v[220:223], v[30:33]
	v_mfma_f32_16x16x32_bf16 v[18:21], v[194:197], v[220:223], v[18:21]
	v_mfma_f32_16x16x32_bf16 v[14:17], v[186:189], v[228:231], v[14:17]
	v_mfma_f32_16x16x32_bf16 v[2:5], v[194:197], v[228:231], v[2:5]
	s_barrier
	s_add_i32 vcc_hi, vcc_hi, 2
	s_add_u32 s97, s97, 0x10000
	s_addc_u32 vcc_lo, vcc_lo, 0
	s_add_u32 s80, s80, 0x100
	s_addc_u32 s81, s81, 0
	s_cmp_gt_u32 vcc_hi, 29
	s_cbranch_scc0 .LBB0_261
	s_and_b64 vcc, exec, s[50:51]
	s_cbranch_vccz .LBB0_264
	s_barrier
	s_setprio 3

.LBB0_277:
	s_setprio 0
	s_andn2_b64 vcc, exec, s[0:1]
	s_mov_b32 s2, s44
	s_mov_b32 s68, s50
	s_mov_b64 s[70:71], s[56:57]
	s_mov_b64 s[72:73], s[54:55]
	s_cbranch_vccz .LBB0_291

.LBB0_285:
	ds_read_b128 v[26:29], v1
	ds_read_b128 v[30:33], v1 offset:1024
	ds_read_b128 v[18:21], v1 offset:2048
	ds_read_b128 v[22:25], v1 offset:3072
	ds_read_b128 v[10:13], v185
	ds_read_b128 v[14:17], v185 offset:1024
	ds_read_b128 v[2:5], v185 offset:2048
	ds_read_b128 v[6:9], v185 offset:3072
	s_add_u32 s26, s70, 0xfffc0080
	s_addc_u32 s27, s71, -1
	s_cmp_eq_u32 s94, 12
	s_cselect_b32 s73, s51, s27
	s_cselect_b32 s72, s90, s26
	s_cselect_b32 s75, s45, s93
	s_cselect_b32 s74, s91, s92
	v_lshl_add_u64 v[176:177], s[70:71], 0, v[168:169]
	s_add_i32 m0, s33, 0xc000
	ds_read_b128 v[190:193], v186
	ds_read_b128 v[194:197], v186 offset:1024
	ds_read_b128 v[198:201], v186 offset:2048
	ds_read_b128 v[202:205], v186 offset:3072
	ds_read_b128 v[206:209], v186 offset:4096
	ds_read_b128 v[210:213], v186 offset:5120
	ds_read_b128 v[220:223], v186 offset:6144
	ds_read_b128 v[224:227], v186 offset:7168
	global_load_lds_dwordx4 v[176:177], off
	v_lshl_add_u64 v[176:177], s[70:71], 0, v[170:171]
	s_add_i32 m0, s33, 0xe000
	s_nop 0
	global_load_lds_dwordx4 v[176:177], off
	s_waitcnt vmcnt(8)
	s_waitcnt lgkmcnt(0)
	s_barrier
	v_mfma_scale_f32_16x16x128_f8f6f4 v[158:161], v[26:33], v[190:197], v[158:161], v187, v188 op_sel_hi:[0,0,0]
	v_mfma_scale_f32_16x16x128_f8f6f4 v[154:157], v[18:25], v[190:197], v[154:157], v187, v188 op_sel_hi:[0,0,0]
	v_mfma_scale_f32_16x16x128_f8f6f4 v[150:153], v[26:33], v[198:205], v[150:153], v187, v188 op_sel_hi:[0,0,0]
	v_mfma_scale_f32_16x16x128_f8f6f4 v[142:145], v[18:25], v[198:205], v[142:145], v187, v188 op_sel_hi:[0,0,0]
	v_mfma_scale_f32_16x16x128_f8f6f4 v[134:137], v[26:33], v[206:213], v[134:137], v187, v188 op_sel_hi:[0,0,0]
	v_mfma_scale_f32_16x16x128_f8f6f4 v[126:129], v[18:25], v[206:213], v[126:129], v187, v188 op_sel_hi:[0,0,0]
	v_mfma_scale_f32_16x16x128_f8f6f4 v[118:121], v[26:33], v[220:227], v[118:121], v187, v188 op_sel_hi:[0,0,0]
	v_mfma_scale_f32_16x16x128_f8f6f4 v[110:113], v[18:25], v[220:227], v[110:113], v187, v188 op_sel_hi:[0,0,0]
	v_mfma_scale_f32_16x16x128_f8f6f4 v[146:149], v[10:17], v[190:197], v[146:149], v187, v188 op_sel_hi:[0,0,0]
	v_mfma_scale_f32_16x16x128_f8f6f4 v[138:141], v[2:9], v[190:197], v[138:141], v187, v188 op_sel_hi:[0,0,0]
	v_mfma_scale_f32_16x16x128_f8f6f4 v[130:133], v[10:17], v[198:205], v[130:133], v187, v188 op_sel_hi:[0,0,0]
	v_mfma_scale_f32_16x16x128_f8f6f4 v[122:125], v[2:9], v[198:205], v[122:125], v187, v188 op_sel_hi:[0,0,0]
	v_mfma_scale_f32_16x16x128_f8f6f4 v[114:117], v[10:17], v[206:213], v[114:117], v187, v188 op_sel_hi:[0,0,0]
	v_mfma_scale_f32_16x16x128_f8f6f4 v[106:109], v[2:9], v[206:213], v[106:109], v187, v188 op_sel_hi:[0,0,0]
	v_mfma_scale_f32_16x16x128_f8f6f4 v[102:105], v[10:17], v[220:227], v[102:105], v187, v188 op_sel_hi:[0,0,0]
	v_mfma_scale_f32_16x16x128_f8f6f4 v[98:101], v[2:9], v[220:227], v[98:101], v187, v188 op_sel_hi:[0,0,0]
	s_barrier
	s_add_i32 s26, s88, s80
	v_lshl_add_u64 v[176:177], s[74:75], 0, v[162:163]
	s_mov_b32 m0, s26
	ds_read_b128 v[190:193], v186 offset:16384
	ds_read_b128 v[194:197], v186 offset:17408
	ds_read_b128 v[198:201], v186 offset:18432
	ds_read_b128 v[202:205], v186 offset:19456
	ds_read_b128 v[206:209], v186 offset:20480
	ds_read_b128 v[210:213], v186 offset:21504
	ds_read_b128 v[220:223], v186 offset:22528
	ds_read_b128 v[224:227], v186 offset:23552
	global_load_lds_dwordx4 v[176:177], off
	v_lshl_add_u64 v[178:179], v[176:177], 0, s[8:9]
	s_add_i32 m0, s26, 0x2000
	s_add_i32 s26, s89, s80
	global_load_lds_dwordx4 v[178:179], off
	v_lshl_add_u64 v[178:179], v[176:177], 0, s[10:11]
	s_mov_b32 m0, s26
	v_lshl_add_u64 v[180:181], s[72:73], 0, v[166:167]
	global_load_lds_dwordx4 v[178:179], off
	v_lshl_add_u64 v[178:179], v[176:177], 0, s[12:13]
	s_add_i32 m0, s26, 0x2000
	s_nop 0
	global_load_lds_dwordx4 v[178:179], off
	v_lshl_add_u64 v[178:179], s[72:73], 0, v[164:165]
	s_mov_b32 m0, s33
	s_nop 0
	global_load_lds_dwordx4 v[178:179], off
	s_mov_b32 m0, s69
	s_nop 0
	global_load_lds_dwordx4 v[180:181], off
	s_waitcnt vmcnt(8)
	s_waitcnt lgkmcnt(0)
	s_barrier
	v_mfma_scale_f32_16x16x128_f8f6f4 v[94:97], v[26:33], v[190:197], v[94:97], v187, v188 op_sel_hi:[0,0,0]
	v_mfma_scale_f32_16x16x128_f8f6f4 v[90:93], v[18:25], v[190:197], v[90:93], v187, v188 op_sel_hi:[0,0,0]
	v_mfma_scale_f32_16x16x128_f8f6f4 v[86:89], v[26:33], v[198:205], v[86:89], v187, v188 op_sel_hi:[0,0,0]
	v_mfma_scale_f32_16x16x128_f8f6f4 v[78:81], v[18:25], v[198:205], v[78:81], v187, v188 op_sel_hi:[0,0,0]
	v_mfma_scale_f32_16x16x128_f8f6f4 v[70:73], v[26:33], v[206:213], v[70:73], v187, v188 op_sel_hi:[0,0,0]
	v_mfma_scale_f32_16x16x128_f8f6f4 v[62:65], v[18:25], v[206:213], v[62:65], v187, v188 op_sel_hi:[0,0,0]
	v_mfma_scale_f32_16x16x128_f8f6f4 v[54:57], v[26:33], v[220:227], v[54:57], v187, v188 op_sel_hi:[0,0,0]
	v_mfma_scale_f32_16x16x128_f8f6f4 v[46:49], v[18:25], v[220:227], v[46:49], v187, v188 op_sel_hi:[0,0,0]
	v_mfma_scale_f32_16x16x128_f8f6f4 v[82:85], v[10:17], v[190:197], v[82:85], v187, v188 op_sel_hi:[0,0,0]
	v_mfma_scale_f32_16x16x128_f8f6f4 v[74:77], v[2:9], v[190:197], v[74:77], v187, v188 op_sel_hi:[0,0,0]
	v_mfma_scale_f32_16x16x128_f8f6f4 v[66:69], v[10:17], v[198:205], v[66:69], v187, v188 op_sel_hi:[0,0,0]
	v_mfma_scale_f32_16x16x128_f8f6f4 v[58:61], v[2:9], v[198:205], v[58:61], v187, v188 op_sel_hi:[0,0,0]
	v_mfma_scale_f32_16x16x128_f8f6f4 v[50:53], v[10:17], v[206:213], v[50:53], v187, v188 op_sel_hi:[0,0,0]
	v_mfma_scale_f32_16x16x128_f8f6f4 v[42:45], v[2:9], v[206:213], v[42:45], v187, v188 op_sel_hi:[0,0,0]
	v_mfma_scale_f32_16x16x128_f8f6f4 v[38:41], v[10:17], v[220:227], v[38:41], v187, v188 op_sel_hi:[0,0,0]
	v_mfma_scale_f32_16x16x128_f8f6f4 v[34:37], v[2:9], v[220:227], v[34:37], v187, v188 op_sel_hi:[0,0,0]
	s_barrier
	s_add_i32 s74, 0, 0x18000
	s_add_i32 s75, 0, 0x1c000
	v_add_u32_e32 v14, s74, v183
	v_add_u32_e32 v30, s75, v183
	ds_read_b128 v[2:5], v14
	ds_read_b128 v[6:9], v14 offset:1024
	ds_read_b128 v[10:13], v14 offset:2048
	ds_read_b128 v[14:17], v14 offset:3072
	ds_read_b128 v[18:21], v30
	ds_read_b128 v[22:25], v30 offset:1024
	ds_read_b128 v[26:29], v30 offset:2048
	ds_read_b128 v[30:33], v30 offset:3072
	s_add_u32 s26, s72, 0x40000
	s_addc_u32 s27, s73, 0
	s_mov_b32 m0, s83
	v_lshl_add_u64 v[214:215], s[26:27], 0, v[164:165]
	ds_read_b128 v[190:193], v186 offset:32768
	ds_read_b128 v[194:197], v186 offset:33792
	ds_read_b128 v[198:201], v186 offset:34816
	ds_read_b128 v[202:205], v186 offset:35840
	ds_read_b128 v[206:209], v186 offset:36864
	ds_read_b128 v[210:213], v186 offset:37888
	ds_read_b128 v[220:223], v186 offset:38912
	ds_read_b128 v[224:227], v186 offset:39936
	global_load_lds_dwordx4 v[214:215], off
	v_lshl_add_u64 v[214:215], s[26:27], 0, v[166:167]
	s_mov_b32 m0, s84
	s_nop 0
	global_load_lds_dwordx4 v[214:215], off
	s_waitcnt vmcnt(8)
	s_waitcnt lgkmcnt(0)
	s_barrier
	v_mfma_scale_f32_16x16x128_f8f6f4 v[158:161], v[2:9], v[190:197], v[158:161], v187, v188 op_sel_hi:[0,0,0]
	v_mfma_scale_f32_16x16x128_f8f6f4 v[154:157], v[10:17], v[190:197], v[154:157], v187, v188 op_sel_hi:[0,0,0]
	v_mfma_scale_f32_16x16x128_f8f6f4 v[150:153], v[2:9], v[198:205], v[150:153], v187, v188 op_sel_hi:[0,0,0]
	v_mfma_scale_f32_16x16x128_f8f6f4 v[142:145], v[10:17], v[198:205], v[142:145], v187, v188 op_sel_hi:[0,0,0]
	v_mfma_scale_f32_16x16x128_f8f6f4 v[134:137], v[2:9], v[206:213], v[134:137], v187, v188 op_sel_hi:[0,0,0]
	v_mfma_scale_f32_16x16x128_f8f6f4 v[126:129], v[10:17], v[206:213], v[126:129], v187, v188 op_sel_hi:[0,0,0]
	v_mfma_scale_f32_16x16x128_f8f6f4 v[118:121], v[2:9], v[220:227], v[118:121], v187, v188 op_sel_hi:[0,0,0]
	v_mfma_scale_f32_16x16x128_f8f6f4 v[110:113], v[10:17], v[220:227], v[110:113], v187, v188 op_sel_hi:[0,0,0]
	v_mfma_scale_f32_16x16x128_f8f6f4 v[146:149], v[18:25], v[190:197], v[146:149], v187, v188 op_sel_hi:[0,0,0]
	v_mfma_scale_f32_16x16x128_f8f6f4 v[138:141], v[26:33], v[190:197], v[138:141], v187, v188 op_sel_hi:[0,0,0]
	v_mfma_scale_f32_16x16x128_f8f6f4 v[130:133], v[18:25], v[198:205], v[130:133], v187, v188 op_sel_hi:[0,0,0]
	v_mfma_scale_f32_16x16x128_f8f6f4 v[122:125], v[26:33], v[198:205], v[122:125], v187, v188 op_sel_hi:[0,0,0]
	v_mfma_scale_f32_16x16x128_f8f6f4 v[114:117], v[18:25], v[206:213], v[114:117], v187, v188 op_sel_hi:[0,0,0]
	v_mfma_scale_f32_16x16x128_f8f6f4 v[106:109], v[26:33], v[206:213], v[106:109], v187, v188 op_sel_hi:[0,0,0]
	v_mfma_scale_f32_16x16x128_f8f6f4 v[102:105], v[18:25], v[220:227], v[102:105], v187, v188 op_sel_hi:[0,0,0]
	v_mfma_scale_f32_16x16x128_f8f6f4 v[98:101], v[26:33], v[220:227], v[98:101], v187, v188 op_sel_hi:[0,0,0]
	s_barrier
	s_add_i32 s26, s74, s80
	v_lshl_add_u64 v[214:215], v[176:177], 0, s[16:17]
	s_mov_b32 m0, s26
	ds_read_b128 v[190:193], v186 offset:49152
	ds_read_b128 v[194:197], v186 offset:50176
	ds_read_b128 v[198:201], v186 offset:51200
	ds_read_b128 v[202:205], v186 offset:52224
	ds_read_b128 v[206:209], v186 offset:53248
	ds_read_b128 v[210:213], v186 offset:54272
	ds_read_b128 v[220:223], v186 offset:55296
	ds_read_b128 v[224:227], v186 offset:56320
	global_load_lds_dwordx4 v[214:215], off
	v_lshl_add_u64 v[214:215], v[176:177], 0, s[18:19]
	s_add_i32 m0, s26, 0x2000
	s_add_i32 s26, s75, s80
	global_load_lds_dwordx4 v[214:215], off
	v_lshl_add_u64 v[214:215], v[176:177], 0, s[22:23]
	s_mov_b32 m0, s26
	v_lshl_add_u64 v[176:177], v[176:177], 0, s[24:25]
	global_load_lds_dwordx4 v[214:215], off
	s_add_i32 m0, s26, 0x2000
	s_nop 0
	global_load_lds_dwordx4 v[176:177], off
	v_lshl_add_u64 v[176:177], v[178:179], 0, s[20:21]
	s_mov_b32 m0, s86
	s_nop 0
	global_load_lds_dwordx4 v[176:177], off
	v_lshl_add_u64 v[176:177], v[180:181], 0, s[20:21]
	s_mov_b32 m0, s87
	s_nop 0
	global_load_lds_dwordx4 v[176:177], off
	s_waitcnt vmcnt(8)
	s_waitcnt lgkmcnt(0)
	s_barrier
	v_mfma_scale_f32_16x16x128_f8f6f4 v[94:97], v[2:9], v[190:197], v[94:97], v187, v188 op_sel_hi:[0,0,0]
	v_mfma_scale_f32_16x16x128_f8f6f4 v[90:93], v[10:17], v[190:197], v[90:93], v187, v188 op_sel_hi:[0,0,0]
	v_mfma_scale_f32_16x16x128_f8f6f4 v[86:89], v[2:9], v[198:205], v[86:89], v187, v188 op_sel_hi:[0,0,0]
	v_mfma_scale_f32_16x16x128_f8f6f4 v[78:81], v[10:17], v[198:205], v[78:81], v187, v188 op_sel_hi:[0,0,0]
	v_mfma_scale_f32_16x16x128_f8f6f4 v[70:73], v[2:9], v[206:213], v[70:73], v187, v188 op_sel_hi:[0,0,0]
	v_mfma_scale_f32_16x16x128_f8f6f4 v[62:65], v[10:17], v[206:213], v[62:65], v187, v188 op_sel_hi:[0,0,0]
	v_mfma_scale_f32_16x16x128_f8f6f4 v[54:57], v[2:9], v[220:227], v[54:57], v187, v188 op_sel_hi:[0,0,0]
	v_mfma_scale_f32_16x16x128_f8f6f4 v[46:49], v[10:17], v[220:227], v[46:49], v187, v188 op_sel_hi:[0,0,0]
	v_mfma_scale_f32_16x16x128_f8f6f4 v[82:85], v[18:25], v[190:197], v[82:85], v187, v188 op_sel_hi:[0,0,0]
	v_mfma_scale_f32_16x16x128_f8f6f4 v[74:77], v[26:33], v[190:197], v[74:77], v187, v188 op_sel_hi:[0,0,0]
	v_mfma_scale_f32_16x16x128_f8f6f4 v[66:69], v[18:25], v[198:205], v[66:69], v187, v188 op_sel_hi:[0,0,0]
	v_mfma_scale_f32_16x16x128_f8f6f4 v[58:61], v[26:33], v[198:205], v[58:61], v187, v188 op_sel_hi:[0,0,0]
	v_mfma_scale_f32_16x16x128_f8f6f4 v[50:53], v[18:25], v[206:213], v[50:53], v187, v188 op_sel_hi:[0,0,0]
	v_mfma_scale_f32_16x16x128_f8f6f4 v[42:45], v[26:33], v[206:213], v[42:45], v187, v188 op_sel_hi:[0,0,0]
	v_mfma_scale_f32_16x16x128_f8f6f4 v[38:41], v[18:25], v[220:227], v[38:41], v187, v188 op_sel_hi:[0,0,0]
	v_mfma_scale_f32_16x16x128_f8f6f4 v[34:37], v[26:33], v[220:227], v[34:37], v187, v188 op_sel_hi:[0,0,0]
	s_barrier
	s_add_i32 s94, s94, 2
	s_add_u32 s92, s92, 0x10000
	s_addc_u32 s93, s93, 0
	s_add_u32 s70, s70, 0x100
	s_addc_u32 s71, s71, 0
	s_cmp_gt_u32 s94, 13
	s_cbranch_scc0 .LBB0_285
	s_and_b64 vcc, exec, s[40:41]
	s_cbranch_vccz .LBB0_288
	s_barrier
	s_setprio 3

.LBB0_652:
	s_setprio 0
	s_andn2_b64 vcc, exec, s[0:1]
	s_mov_b32 s2, s40
	s_mov_b32 s56, s44
	s_mov_b64 s[58:59], s[54:55]
	s_mov_b64 s[60:61], s[50:51]
	s_cbranch_vccz .LBB0_666

.LBB0_660:
	ds_read_b128 v[130:133], v222
	ds_read_b128 v[134:137], v222 offset:1024
	ds_read_b128 v[138:141], v222 offset:2048
	ds_read_b128 v[142:145], v222 offset:3072
	ds_read_b128 v[146:149], v223
	ds_read_b128 v[150:153], v223 offset:1024
	ds_read_b128 v[154:157], v223 offset:2048
	ds_read_b128 v[158:161], v223 offset:3072
	s_add_u32 s26, s58, 0xfff80080
	s_addc_u32 s27, s59, -1
	s_cmp_eq_u32 s80, 28
	s_cselect_b32 s61, s45, s27
	s_cselect_b32 s60, s72, s26
	s_cselect_b32 s27, s41, s75
	s_cselect_b32 s26, s73, s74
	v_lshl_add_u64 v[208:209], s[58:59], 0, v[200:201]
	s_add_i32 m0, s57, 0xc000
	ds_read_b128 v[162:165], v224
	ds_read_b128 v[166:169], v224 offset:1024
	ds_read_b128 v[170:173], v224 offset:2048
	ds_read_b128 v[174:177], v224 offset:3072
	ds_read_b128 v[178:181], v224 offset:4096
	ds_read_b128 v[182:185], v224 offset:5120
	ds_read_b128 v[186:189], v224 offset:6144
	ds_read_b128 v[190:193], v224 offset:7168
	global_load_lds_dwordx4 v[208:209], off
	v_lshl_add_u64 v[208:209], s[58:59], 0, v[202:203]
	s_add_i32 m0, s57, 0xe000
	s_nop 0
	global_load_lds_dwordx4 v[208:209], off
	s_waitcnt vmcnt(8)
	s_waitcnt lgkmcnt(0)
	s_barrier
	v_mfma_f32_16x16x32_bf16 v[126:129], v[130:133], v[162:165], v[126:129]
	v_mfma_f32_16x16x32_bf16 v[122:125], v[138:141], v[162:165], v[122:125]
	v_mfma_f32_16x16x32_bf16 v[118:121], v[130:133], v[170:173], v[118:121]
	v_mfma_f32_16x16x32_bf16 v[114:117], v[138:141], v[170:173], v[114:117]
	v_mfma_f32_16x16x32_bf16 v[110:113], v[130:133], v[178:181], v[110:113]
	v_mfma_f32_16x16x32_bf16 v[102:105], v[138:141], v[178:181], v[102:105]
	v_mfma_f32_16x16x32_bf16 v[94:97], v[130:133], v[186:189], v[94:97]
	v_mfma_f32_16x16x32_bf16 v[74:77], v[138:141], v[186:189], v[74:77]
	v_mfma_f32_16x16x32_bf16 v[126:129], v[134:137], v[166:169], v[126:129]
	v_mfma_f32_16x16x32_bf16 v[122:125], v[142:145], v[166:169], v[122:125]
	v_mfma_f32_16x16x32_bf16 v[118:121], v[134:137], v[174:177], v[118:121]
	v_mfma_f32_16x16x32_bf16 v[114:117], v[142:145], v[174:177], v[114:117]
	v_mfma_f32_16x16x32_bf16 v[110:113], v[134:137], v[182:185], v[110:113]
	v_mfma_f32_16x16x32_bf16 v[102:105], v[142:145], v[182:185], v[102:105]
	v_mfma_f32_16x16x32_bf16 v[94:97], v[134:137], v[190:193], v[94:97]
	v_mfma_f32_16x16x32_bf16 v[74:77], v[142:145], v[190:193], v[74:77]
	v_mfma_f32_16x16x32_bf16 v[106:109], v[146:149], v[162:165], v[106:109]
	v_mfma_f32_16x16x32_bf16 v[98:101], v[154:157], v[162:165], v[98:101]
	v_mfma_f32_16x16x32_bf16 v[90:93], v[146:149], v[170:173], v[90:93]
	v_mfma_f32_16x16x32_bf16 v[86:89], v[154:157], v[170:173], v[86:89]
	v_mfma_f32_16x16x32_bf16 v[82:85], v[146:149], v[178:181], v[82:85]
	v_mfma_f32_16x16x32_bf16 v[78:81], v[154:157], v[178:181], v[78:81]
	v_mfma_f32_16x16x32_bf16 v[70:73], v[146:149], v[186:189], v[70:73]
	v_mfma_f32_16x16x32_bf16 v[66:69], v[154:157], v[186:189], v[66:69]
	v_mfma_f32_16x16x32_bf16 v[106:109], v[150:153], v[166:169], v[106:109]
	v_mfma_f32_16x16x32_bf16 v[98:101], v[158:161], v[166:169], v[98:101]
	v_mfma_f32_16x16x32_bf16 v[90:93], v[150:153], v[174:177], v[90:93]
	v_mfma_f32_16x16x32_bf16 v[86:89], v[158:161], v[174:177], v[86:89]
	v_mfma_f32_16x16x32_bf16 v[82:85], v[150:153], v[182:185], v[82:85]
	v_mfma_f32_16x16x32_bf16 v[78:81], v[158:161], v[182:185], v[78:81]
	v_mfma_f32_16x16x32_bf16 v[70:73], v[150:153], v[190:193], v[70:73]
	v_mfma_f32_16x16x32_bf16 v[66:69], v[158:161], v[190:193], v[66:69]
	s_barrier
	v_lshl_add_u64 v[208:209], s[26:27], 0, v[194:195]
	s_add_i32 s26, s70, s35
	s_mov_b32 m0, s26
	ds_read_b128 v[162:165], v224 offset:16384
	ds_read_b128 v[166:169], v224 offset:17408
	ds_read_b128 v[170:173], v224 offset:18432
	ds_read_b128 v[174:177], v224 offset:19456
	ds_read_b128 v[178:181], v224 offset:20480
	ds_read_b128 v[182:185], v224 offset:21504
	ds_read_b128 v[186:189], v224 offset:22528
	ds_read_b128 v[190:193], v224 offset:23552
	global_load_lds_dwordx4 v[208:209], off
	v_lshl_add_u64 v[210:211], v[208:209], 0, s[6:7]
	s_add_i32 m0, s26, 0x2000
	s_add_i32 s26, s71, s35
	global_load_lds_dwordx4 v[210:211], off
	v_lshl_add_u64 v[210:211], v[208:209], 0, s[8:9]
	s_mov_b32 m0, s26
	v_lshl_add_u64 v[212:213], s[60:61], 0, v[198:199]
	global_load_lds_dwordx4 v[210:211], off
	v_lshl_add_u64 v[210:211], v[208:209], 0, s[10:11]
	s_add_i32 m0, s26, 0x2000
	s_nop 0
	global_load_lds_dwordx4 v[210:211], off
	v_lshl_add_u64 v[210:211], s[60:61], 0, v[196:197]
	s_mov_b32 m0, s57
	s_nop 0
	global_load_lds_dwordx4 v[210:211], off
	s_mov_b32 m0, s63
	s_nop 0
	global_load_lds_dwordx4 v[212:213], off
	s_waitcnt vmcnt(8)
	s_waitcnt lgkmcnt(0)
	s_barrier
	v_mfma_f32_16x16x32_bf16 v[62:65], v[130:133], v[162:165], v[62:65]
	v_mfma_f32_16x16x32_bf16 v[58:61], v[138:141], v[162:165], v[58:61]
	v_mfma_f32_16x16x32_bf16 v[54:57], v[130:133], v[170:173], v[54:57]
	v_mfma_f32_16x16x32_bf16 v[50:53], v[138:141], v[170:173], v[50:53]
	v_mfma_f32_16x16x32_bf16 v[46:49], v[130:133], v[178:181], v[46:49]
	v_mfma_f32_16x16x32_bf16 v[38:41], v[138:141], v[178:181], v[38:41]
	v_mfma_f32_16x16x32_bf16 v[30:33], v[130:133], v[186:189], v[30:33]
	v_mfma_f32_16x16x32_bf16 v[10:13], v[138:141], v[186:189], v[10:13]
	v_mfma_f32_16x16x32_bf16 v[62:65], v[134:137], v[166:169], v[62:65]
	v_mfma_f32_16x16x32_bf16 v[58:61], v[142:145], v[166:169], v[58:61]
	v_mfma_f32_16x16x32_bf16 v[54:57], v[134:137], v[174:177], v[54:57]
	v_mfma_f32_16x16x32_bf16 v[50:53], v[142:145], v[174:177], v[50:53]
	v_mfma_f32_16x16x32_bf16 v[46:49], v[134:137], v[182:185], v[46:49]
	v_mfma_f32_16x16x32_bf16 v[38:41], v[142:145], v[182:185], v[38:41]
	v_mfma_f32_16x16x32_bf16 v[30:33], v[134:137], v[190:193], v[30:33]
	v_mfma_f32_16x16x32_bf16 v[10:13], v[142:145], v[190:193], v[10:13]
	v_mfma_f32_16x16x32_bf16 v[42:45], v[146:149], v[162:165], v[42:45]
	v_mfma_f32_16x16x32_bf16 v[34:37], v[154:157], v[162:165], v[34:37]
	v_mfma_f32_16x16x32_bf16 v[26:29], v[146:149], v[170:173], v[26:29]
	v_mfma_f32_16x16x32_bf16 v[22:25], v[154:157], v[170:173], v[22:25]
	v_mfma_f32_16x16x32_bf16 v[18:21], v[146:149], v[178:181], v[18:21]
	v_mfma_f32_16x16x32_bf16 v[14:17], v[154:157], v[178:181], v[14:17]
	v_mfma_f32_16x16x32_bf16 v[6:9], v[146:149], v[186:189], v[6:9]
	v_mfma_f32_16x16x32_bf16 v[2:5], v[154:157], v[186:189], v[2:5]
	v_mfma_f32_16x16x32_bf16 v[42:45], v[150:153], v[166:169], v[42:45]
	v_mfma_f32_16x16x32_bf16 v[34:37], v[158:161], v[166:169], v[34:37]
	v_mfma_f32_16x16x32_bf16 v[26:29], v[150:153], v[174:177], v[26:29]
	v_mfma_f32_16x16x32_bf16 v[22:25], v[158:161], v[174:177], v[22:25]
	v_mfma_f32_16x16x32_bf16 v[18:21], v[150:153], v[182:185], v[18:21]
	v_mfma_f32_16x16x32_bf16 v[14:17], v[158:161], v[182:185], v[14:17]
	v_mfma_f32_16x16x32_bf16 v[6:9], v[150:153], v[190:193], v[6:9]
	v_mfma_f32_16x16x32_bf16 v[2:5], v[158:161], v[190:193], v[2:5]
	s_barrier
	s_add_i32 s81, 0, 0x18000
	s_add_i32 s82, 0, 0x1c000
	v_add_u32_e32 v142, s81, v220
	v_add_u32_e32 v158, s82, v220
	ds_read_b128 v[130:133], v142
	ds_read_b128 v[134:137], v142 offset:1024
	ds_read_b128 v[138:141], v142 offset:2048
	ds_read_b128 v[142:145], v142 offset:3072
	ds_read_b128 v[146:149], v158
	ds_read_b128 v[150:153], v158 offset:1024
	ds_read_b128 v[154:157], v158 offset:2048
	ds_read_b128 v[158:161], v158 offset:3072
	s_add_u32 s26, s60, 0x80000
	s_addc_u32 s27, s61, 0
	s_mov_b32 m0, s64
	v_lshl_add_u64 v[214:215], s[26:27], 0, v[196:197]
	ds_read_b128 v[162:165], v224 offset:32768
	ds_read_b128 v[166:169], v224 offset:33792
	ds_read_b128 v[170:173], v224 offset:34816
	ds_read_b128 v[174:177], v224 offset:35840
	ds_read_b128 v[178:181], v224 offset:36864
	ds_read_b128 v[182:185], v224 offset:37888
	ds_read_b128 v[186:189], v224 offset:38912
	ds_read_b128 v[190:193], v224 offset:39936
	global_load_lds_dwordx4 v[214:215], off
	v_lshl_add_u64 v[214:215], s[26:27], 0, v[198:199]
	s_mov_b32 m0, s65
	s_nop 0
	global_load_lds_dwordx4 v[214:215], off
	s_waitcnt vmcnt(8)
	s_waitcnt lgkmcnt(0)
	s_barrier
	v_mfma_f32_16x16x32_bf16 v[126:129], v[130:133], v[162:165], v[126:129]
	v_mfma_f32_16x16x32_bf16 v[122:125], v[138:141], v[162:165], v[122:125]
	v_mfma_f32_16x16x32_bf16 v[118:121], v[130:133], v[170:173], v[118:121]
	v_mfma_f32_16x16x32_bf16 v[114:117], v[138:141], v[170:173], v[114:117]
	v_mfma_f32_16x16x32_bf16 v[110:113], v[130:133], v[178:181], v[110:113]
	v_mfma_f32_16x16x32_bf16 v[102:105], v[138:141], v[178:181], v[102:105]
	v_mfma_f32_16x16x32_bf16 v[94:97], v[130:133], v[186:189], v[94:97]
	v_mfma_f32_16x16x32_bf16 v[74:77], v[138:141], v[186:189], v[74:77]
	v_mfma_f32_16x16x32_bf16 v[126:129], v[134:137], v[166:169], v[126:129]
	v_mfma_f32_16x16x32_bf16 v[122:125], v[142:145], v[166:169], v[122:125]
	v_mfma_f32_16x16x32_bf16 v[118:121], v[134:137], v[174:177], v[118:121]
	v_mfma_f32_16x16x32_bf16 v[114:117], v[142:145], v[174:177], v[114:117]
	v_mfma_f32_16x16x32_bf16 v[110:113], v[134:137], v[182:185], v[110:113]
	v_mfma_f32_16x16x32_bf16 v[102:105], v[142:145], v[182:185], v[102:105]
	v_mfma_f32_16x16x32_bf16 v[94:97], v[134:137], v[190:193], v[94:97]
	v_mfma_f32_16x16x32_bf16 v[74:77], v[142:145], v[190:193], v[74:77]
	v_mfma_f32_16x16x32_bf16 v[106:109], v[146:149], v[162:165], v[106:109]
	v_mfma_f32_16x16x32_bf16 v[98:101], v[154:157], v[162:165], v[98:101]
	v_mfma_f32_16x16x32_bf16 v[90:93], v[146:149], v[170:173], v[90:93]
	v_mfma_f32_16x16x32_bf16 v[86:89], v[154:157], v[170:173], v[86:89]
	v_mfma_f32_16x16x32_bf16 v[82:85], v[146:149], v[178:181], v[82:85]
	v_mfma_f32_16x16x32_bf16 v[78:81], v[154:157], v[178:181], v[78:81]
	v_mfma_f32_16x16x32_bf16 v[70:73], v[146:149], v[186:189], v[70:73]
	v_mfma_f32_16x16x32_bf16 v[66:69], v[154:157], v[186:189], v[66:69]
	v_mfma_f32_16x16x32_bf16 v[106:109], v[150:153], v[166:169], v[106:109]
	v_mfma_f32_16x16x32_bf16 v[98:101], v[158:161], v[166:169], v[98:101]
	v_mfma_f32_16x16x32_bf16 v[90:93], v[150:153], v[174:177], v[90:93]
	v_mfma_f32_16x16x32_bf16 v[86:89], v[158:161], v[174:177], v[86:89]
	v_mfma_f32_16x16x32_bf16 v[82:85], v[150:153], v[182:185], v[82:85]
	v_mfma_f32_16x16x32_bf16 v[78:81], v[158:161], v[182:185], v[78:81]
	v_mfma_f32_16x16x32_bf16 v[70:73], v[150:153], v[190:193], v[70:73]
	v_mfma_f32_16x16x32_bf16 v[66:69], v[158:161], v[190:193], v[66:69]
	s_barrier
	s_add_i32 s26, s81, s35
	v_lshl_add_u64 v[214:215], v[208:209], 0, s[14:15]
	s_mov_b32 m0, s26
	ds_read_b128 v[162:165], v224 offset:49152
	ds_read_b128 v[166:169], v224 offset:50176
	ds_read_b128 v[170:173], v224 offset:51200
	ds_read_b128 v[174:177], v224 offset:52224
	ds_read_b128 v[178:181], v224 offset:53248
	ds_read_b128 v[182:185], v224 offset:54272
	ds_read_b128 v[186:189], v224 offset:55296
	ds_read_b128 v[190:193], v224 offset:56320
	global_load_lds_dwordx4 v[214:215], off
	v_lshl_add_u64 v[214:215], v[208:209], 0, s[16:17]
	s_add_i32 m0, s26, 0x2000
	s_add_i32 s26, s82, s35
	global_load_lds_dwordx4 v[214:215], off
	v_lshl_add_u64 v[214:215], v[208:209], 0, s[20:21]
	s_mov_b32 m0, s26
	v_lshl_add_u64 v[208:209], v[208:209], 0, s[22:23]
	global_load_lds_dwordx4 v[214:215], off
	s_add_i32 m0, s26, 0x2000
	s_nop 0
	global_load_lds_dwordx4 v[208:209], off
	v_lshl_add_u64 v[208:209], v[210:211], 0, s[18:19]
	s_mov_b32 m0, s67
	s_nop 0
	global_load_lds_dwordx4 v[208:209], off
	v_lshl_add_u64 v[208:209], v[212:213], 0, s[18:19]
	s_mov_b32 m0, s68
	s_nop 0
	global_load_lds_dwordx4 v[208:209], off
	s_waitcnt vmcnt(8)
	s_waitcnt lgkmcnt(0)
	s_barrier
	v_mfma_f32_16x16x32_bf16 v[62:65], v[130:133], v[162:165], v[62:65]
	v_mfma_f32_16x16x32_bf16 v[58:61], v[138:141], v[162:165], v[58:61]
	v_mfma_f32_16x16x32_bf16 v[54:57], v[130:133], v[170:173], v[54:57]
	v_mfma_f32_16x16x32_bf16 v[50:53], v[138:141], v[170:173], v[50:53]
	v_mfma_f32_16x16x32_bf16 v[46:49], v[130:133], v[178:181], v[46:49]
	v_mfma_f32_16x16x32_bf16 v[38:41], v[138:141], v[178:181], v[38:41]
	v_mfma_f32_16x16x32_bf16 v[30:33], v[130:133], v[186:189], v[30:33]
	v_mfma_f32_16x16x32_bf16 v[10:13], v[138:141], v[186:189], v[10:13]
	v_mfma_f32_16x16x32_bf16 v[62:65], v[134:137], v[166:169], v[62:65]
	v_mfma_f32_16x16x32_bf16 v[58:61], v[142:145], v[166:169], v[58:61]
	v_mfma_f32_16x16x32_bf16 v[54:57], v[134:137], v[174:177], v[54:57]
	v_mfma_f32_16x16x32_bf16 v[50:53], v[142:145], v[174:177], v[50:53]
	v_mfma_f32_16x16x32_bf16 v[46:49], v[134:137], v[182:185], v[46:49]
	v_mfma_f32_16x16x32_bf16 v[38:41], v[142:145], v[182:185], v[38:41]
	v_mfma_f32_16x16x32_bf16 v[30:33], v[134:137], v[190:193], v[30:33]
	v_mfma_f32_16x16x32_bf16 v[10:13], v[142:145], v[190:193], v[10:13]
	v_mfma_f32_16x16x32_bf16 v[42:45], v[146:149], v[162:165], v[42:45]
	v_mfma_f32_16x16x32_bf16 v[34:37], v[154:157], v[162:165], v[34:37]
	v_mfma_f32_16x16x32_bf16 v[26:29], v[146:149], v[170:173], v[26:29]
	v_mfma_f32_16x16x32_bf16 v[22:25], v[154:157], v[170:173], v[22:25]
	v_mfma_f32_16x16x32_bf16 v[18:21], v[146:149], v[178:181], v[18:21]
	v_mfma_f32_16x16x32_bf16 v[14:17], v[154:157], v[178:181], v[14:17]
	v_mfma_f32_16x16x32_bf16 v[6:9], v[146:149], v[186:189], v[6:9]
	v_mfma_f32_16x16x32_bf16 v[2:5], v[154:157], v[186:189], v[2:5]
	v_mfma_f32_16x16x32_bf16 v[42:45], v[150:153], v[166:169], v[42:45]
	v_mfma_f32_16x16x32_bf16 v[34:37], v[158:161], v[166:169], v[34:37]
	v_mfma_f32_16x16x32_bf16 v[26:29], v[150:153], v[174:177], v[26:29]
	v_mfma_f32_16x16x32_bf16 v[22:25], v[158:161], v[174:177], v[22:25]
	v_mfma_f32_16x16x32_bf16 v[18:21], v[150:153], v[182:185], v[18:21]
	v_mfma_f32_16x16x32_bf16 v[14:17], v[158:161], v[182:185], v[14:17]
	v_mfma_f32_16x16x32_bf16 v[6:9], v[150:153], v[190:193], v[6:9]
	v_mfma_f32_16x16x32_bf16 v[2:5], v[158:161], v[190:193], v[2:5]
	s_barrier
	s_add_i32 s80, s80, 2
	s_add_u32 s74, s74, 0x10000
	s_addc_u32 s75, s75, 0
	s_add_u32 s58, s58, 0x100
	s_addc_u32 s59, s59, 0
	s_cmp_gt_u32 s80, 29
	s_cbranch_scc0 .LBB0_660
	s_and_b64 vcc, exec, s[24:25]
	s_cbranch_vccz .LBB0_663
	s_barrier
	s_setprio 3

.LBB0_779:
	s_setprio 0
	s_andn2_b64 vcc, exec, s[0:1]
	s_mov_b32 s2, s52
	s_mov_b32 s60, s54
	s_mov_b64 s[62:63], s[58:59]
	s_mov_b64 s[64:65], s[56:57]
	s_cbranch_vccz .LBB0_789

.LBB0_783:
	ds_read_b128 v[144:147], v151
	ds_read_b128 v[156:159], v151 offset:1024
	ds_read_b128 v[160:163], v151 offset:2048
	ds_read_b128 v[164:167], v151 offset:3072
	ds_read_b128 v[168:171], v152
	ds_read_b128 v[172:175], v152 offset:1024
	ds_read_b128 v[176:179], v152 offset:2048
	ds_read_b128 v[180:183], v152 offset:3072
	s_add_u32 s26, s62, 0xfff80080
	s_addc_u32 s27, s63, -1
	s_cmp_eq_u32 s85, 28
	s_cselect_b32 s65, s55, s27
	s_cselect_b32 s64, s81, s26
	s_cselect_b32 s27, s53, s84
	s_cselect_b32 s26, s82, s83
	v_lshl_add_u64 v[216:217], s[62:63], 0, v[136:137]
	s_add_i32 m0, s61, 0xc000
	ds_read_b128 v[184:187], v153
	ds_read_b128 v[188:191], v153 offset:1024
	ds_read_b128 v[192:195], v153 offset:2048
	ds_read_b128 v[196:199], v153 offset:3072
	ds_read_b128 v[200:203], v153 offset:4096
	ds_read_b128 v[204:207], v153 offset:5120
	ds_read_b128 v[208:211], v153 offset:6144
	ds_read_b128 v[212:215], v153 offset:7168
	global_load_lds_dwordx4 v[216:217], off
	v_lshl_add_u64 v[216:217], s[62:63], 0, v[138:139]
	s_add_i32 m0, s61, 0xe000
	s_nop 0
	global_load_lds_dwordx4 v[216:217], off
	s_waitcnt vmcnt(8)
	s_waitcnt lgkmcnt(0)
	s_barrier
	v_mfma_f32_16x16x32_bf16 v[126:129], v[144:147], v[184:187], v[126:129]
	v_mfma_f32_16x16x32_bf16 v[118:121], v[160:163], v[184:187], v[118:121]
	v_mfma_f32_16x16x32_bf16 v[110:113], v[144:147], v[192:195], v[110:113]
	v_mfma_f32_16x16x32_bf16 v[102:105], v[160:163], v[192:195], v[102:105]
	v_mfma_f32_16x16x32_bf16 v[94:97], v[144:147], v[200:203], v[94:97]
	v_mfma_f32_16x16x32_bf16 v[86:89], v[160:163], v[200:203], v[86:89]
	v_mfma_f32_16x16x32_bf16 v[78:81], v[144:147], v[208:211], v[78:81]
	v_mfma_f32_16x16x32_bf16 v[70:73], v[160:163], v[208:211], v[70:73]
	v_mfma_f32_16x16x32_bf16 v[126:129], v[156:159], v[188:191], v[126:129]
	v_mfma_f32_16x16x32_bf16 v[118:121], v[164:167], v[188:191], v[118:121]
	v_mfma_f32_16x16x32_bf16 v[110:113], v[156:159], v[196:199], v[110:113]
	v_mfma_f32_16x16x32_bf16 v[102:105], v[164:167], v[196:199], v[102:105]
	v_mfma_f32_16x16x32_bf16 v[94:97], v[156:159], v[204:207], v[94:97]
	v_mfma_f32_16x16x32_bf16 v[86:89], v[164:167], v[204:207], v[86:89]
	v_mfma_f32_16x16x32_bf16 v[78:81], v[156:159], v[212:215], v[78:81]
	v_mfma_f32_16x16x32_bf16 v[70:73], v[164:167], v[212:215], v[70:73]
	v_mfma_f32_16x16x32_bf16 v[122:125], v[168:171], v[184:187], v[122:125]
	v_mfma_f32_16x16x32_bf16 v[114:117], v[176:179], v[184:187], v[114:117]
	v_mfma_f32_16x16x32_bf16 v[106:109], v[168:171], v[192:195], v[106:109]
	v_mfma_f32_16x16x32_bf16 v[98:101], v[176:179], v[192:195], v[98:101]
	v_mfma_f32_16x16x32_bf16 v[90:93], v[168:171], v[200:203], v[90:93]
	v_mfma_f32_16x16x32_bf16 v[82:85], v[176:179], v[200:203], v[82:85]
	v_mfma_f32_16x16x32_bf16 v[74:77], v[168:171], v[208:211], v[74:77]
	v_mfma_f32_16x16x32_bf16 v[66:69], v[176:179], v[208:211], v[66:69]
	v_mfma_f32_16x16x32_bf16 v[122:125], v[172:175], v[188:191], v[122:125]
	v_mfma_f32_16x16x32_bf16 v[114:117], v[180:183], v[188:191], v[114:117]
	v_mfma_f32_16x16x32_bf16 v[106:109], v[172:175], v[196:199], v[106:109]
	v_mfma_f32_16x16x32_bf16 v[98:101], v[180:183], v[196:199], v[98:101]
	v_mfma_f32_16x16x32_bf16 v[90:93], v[172:175], v[204:207], v[90:93]
	v_mfma_f32_16x16x32_bf16 v[82:85], v[180:183], v[204:207], v[82:85]
	v_mfma_f32_16x16x32_bf16 v[74:77], v[172:175], v[212:215], v[74:77]
	v_mfma_f32_16x16x32_bf16 v[66:69], v[180:183], v[212:215], v[66:69]
	s_barrier
	v_lshl_add_u64 v[216:217], s[26:27], 0, v[130:131]
	s_add_i32 s26, s73, s35
	s_mov_b32 m0, s26
	ds_read_b128 v[184:187], v153 offset:16384
	ds_read_b128 v[188:191], v153 offset:17408
	ds_read_b128 v[192:195], v153 offset:18432
	ds_read_b128 v[196:199], v153 offset:19456
	ds_read_b128 v[200:203], v153 offset:20480
	ds_read_b128 v[204:207], v153 offset:21504
	ds_read_b128 v[208:211], v153 offset:22528
	ds_read_b128 v[212:215], v153 offset:23552
	global_load_lds_dwordx4 v[216:217], off
	v_lshl_add_u64 v[220:221], v[216:217], 0, s[6:7]
	s_add_i32 m0, s26, 0x2000
	s_add_i32 s26, s74, s35
	global_load_lds_dwordx4 v[220:221], off
	v_lshl_add_u64 v[220:221], v[216:217], 0, s[8:9]
	s_mov_b32 m0, s26
	v_lshl_add_u64 v[222:223], s[64:65], 0, v[134:135]
	global_load_lds_dwordx4 v[220:221], off
	v_lshl_add_u64 v[220:221], v[216:217], 0, s[10:11]
	s_add_i32 m0, s26, 0x2000
	s_nop 0
	global_load_lds_dwordx4 v[220:221], off
	v_lshl_add_u64 v[220:221], s[64:65], 0, v[132:133]
	s_mov_b32 m0, s61
	s_nop 0
	global_load_lds_dwordx4 v[220:221], off
	s_mov_b32 m0, s66
	s_nop 0
	global_load_lds_dwordx4 v[222:223], off
	s_waitcnt vmcnt(8)
	s_waitcnt lgkmcnt(0)
	s_barrier
	v_mfma_f32_16x16x32_bf16 v[62:65], v[144:147], v[184:187], v[62:65]
	v_mfma_f32_16x16x32_bf16 v[54:57], v[160:163], v[184:187], v[54:57]
	v_mfma_f32_16x16x32_bf16 v[46:49], v[144:147], v[192:195], v[46:49]
	v_mfma_f32_16x16x32_bf16 v[38:41], v[160:163], v[192:195], v[38:41]
	v_mfma_f32_16x16x32_bf16 v[30:33], v[144:147], v[200:203], v[30:33]
	v_mfma_f32_16x16x32_bf16 v[22:25], v[160:163], v[200:203], v[22:25]
	v_mfma_f32_16x16x32_bf16 v[14:17], v[144:147], v[208:211], v[14:17]
	v_mfma_f32_16x16x32_bf16 v[6:9], v[160:163], v[208:211], v[6:9]
	v_mfma_f32_16x16x32_bf16 v[62:65], v[156:159], v[188:191], v[62:65]
	v_mfma_f32_16x16x32_bf16 v[54:57], v[164:167], v[188:191], v[54:57]
	v_mfma_f32_16x16x32_bf16 v[46:49], v[156:159], v[196:199], v[46:49]
	v_mfma_f32_16x16x32_bf16 v[38:41], v[164:167], v[196:199], v[38:41]
	v_mfma_f32_16x16x32_bf16 v[30:33], v[156:159], v[204:207], v[30:33]
	v_mfma_f32_16x16x32_bf16 v[22:25], v[164:167], v[204:207], v[22:25]
	v_mfma_f32_16x16x32_bf16 v[14:17], v[156:159], v[212:215], v[14:17]
	v_mfma_f32_16x16x32_bf16 v[6:9], v[164:167], v[212:215], v[6:9]
	v_mfma_f32_16x16x32_bf16 v[58:61], v[168:171], v[184:187], v[58:61]
	v_mfma_f32_16x16x32_bf16 v[50:53], v[176:179], v[184:187], v[50:53]
	v_mfma_f32_16x16x32_bf16 v[42:45], v[168:171], v[192:195], v[42:45]
	v_mfma_f32_16x16x32_bf16 v[34:37], v[176:179], v[192:195], v[34:37]
	v_mfma_f32_16x16x32_bf16 v[26:29], v[168:171], v[200:203], v[26:29]
	v_mfma_f32_16x16x32_bf16 v[18:21], v[176:179], v[200:203], v[18:21]
	v_mfma_f32_16x16x32_bf16 v[10:13], v[168:171], v[208:211], v[10:13]
	v_mfma_f32_16x16x32_bf16 v[2:5], v[176:179], v[208:211], v[2:5]
	v_mfma_f32_16x16x32_bf16 v[58:61], v[172:175], v[188:191], v[58:61]
	v_mfma_f32_16x16x32_bf16 v[50:53], v[180:183], v[188:191], v[50:53]
	v_mfma_f32_16x16x32_bf16 v[42:45], v[172:175], v[196:199], v[42:45]
	v_mfma_f32_16x16x32_bf16 v[34:37], v[180:183], v[196:199], v[34:37]
	v_mfma_f32_16x16x32_bf16 v[26:29], v[172:175], v[204:207], v[26:29]
	v_mfma_f32_16x16x32_bf16 v[18:21], v[180:183], v[204:207], v[18:21]
	v_mfma_f32_16x16x32_bf16 v[10:13], v[172:175], v[212:215], v[10:13]
	v_mfma_f32_16x16x32_bf16 v[2:5], v[180:183], v[212:215], v[2:5]
	s_barrier
	s_add_i32 s86, 0, 0x18000
	v_add_u32_e32 v155, s86, v149
	s_add_i32 s87, 0, 0x1c000
	ds_read_b128 v[144:147], v155
	ds_read_b128 v[156:159], v155 offset:1024
	ds_read_b128 v[160:163], v155 offset:2048
	ds_read_b128 v[164:167], v155 offset:3072
	v_add_u32_e32 v155, s87, v149
	ds_read_b128 v[168:171], v155
	ds_read_b128 v[172:175], v155 offset:1024
	ds_read_b128 v[176:179], v155 offset:2048
	ds_read_b128 v[180:183], v155 offset:3072
	s_add_u32 s26, s64, 0x80000
	s_addc_u32 s27, s65, 0
	s_mov_b32 m0, s67
	v_lshl_add_u64 v[224:225], s[26:27], 0, v[132:133]
	ds_read_b128 v[184:187], v153 offset:32768
	ds_read_b128 v[188:191], v153 offset:33792
	ds_read_b128 v[192:195], v153 offset:34816
	ds_read_b128 v[196:199], v153 offset:35840
	ds_read_b128 v[200:203], v153 offset:36864
	ds_read_b128 v[204:207], v153 offset:37888
	ds_read_b128 v[208:211], v153 offset:38912
	ds_read_b128 v[212:215], v153 offset:39936
	global_load_lds_dwordx4 v[224:225], off
	v_lshl_add_u64 v[224:225], s[26:27], 0, v[134:135]
	s_mov_b32 m0, s68
	s_nop 0
	global_load_lds_dwordx4 v[224:225], off
	s_waitcnt vmcnt(8)
	s_waitcnt lgkmcnt(0)
	s_barrier
	v_mfma_f32_16x16x32_bf16 v[126:129], v[144:147], v[184:187], v[126:129]
	v_mfma_f32_16x16x32_bf16 v[118:121], v[160:163], v[184:187], v[118:121]
	v_mfma_f32_16x16x32_bf16 v[110:113], v[144:147], v[192:195], v[110:113]
	v_mfma_f32_16x16x32_bf16 v[102:105], v[160:163], v[192:195], v[102:105]
	v_mfma_f32_16x16x32_bf16 v[94:97], v[144:147], v[200:203], v[94:97]
	v_mfma_f32_16x16x32_bf16 v[86:89], v[160:163], v[200:203], v[86:89]
	v_mfma_f32_16x16x32_bf16 v[78:81], v[144:147], v[208:211], v[78:81]
	v_mfma_f32_16x16x32_bf16 v[70:73], v[160:163], v[208:211], v[70:73]
	v_mfma_f32_16x16x32_bf16 v[126:129], v[156:159], v[188:191], v[126:129]
	v_mfma_f32_16x16x32_bf16 v[118:121], v[164:167], v[188:191], v[118:121]
	v_mfma_f32_16x16x32_bf16 v[110:113], v[156:159], v[196:199], v[110:113]
	v_mfma_f32_16x16x32_bf16 v[102:105], v[164:167], v[196:199], v[102:105]
	v_mfma_f32_16x16x32_bf16 v[94:97], v[156:159], v[204:207], v[94:97]
	v_mfma_f32_16x16x32_bf16 v[86:89], v[164:167], v[204:207], v[86:89]
	v_mfma_f32_16x16x32_bf16 v[78:81], v[156:159], v[212:215], v[78:81]
	v_mfma_f32_16x16x32_bf16 v[70:73], v[164:167], v[212:215], v[70:73]
	v_mfma_f32_16x16x32_bf16 v[122:125], v[168:171], v[184:187], v[122:125]
	v_mfma_f32_16x16x32_bf16 v[114:117], v[176:179], v[184:187], v[114:117]
	v_mfma_f32_16x16x32_bf16 v[106:109], v[168:171], v[192:195], v[106:109]
	v_mfma_f32_16x16x32_bf16 v[98:101], v[176:179], v[192:195], v[98:101]
	v_mfma_f32_16x16x32_bf16 v[90:93], v[168:171], v[200:203], v[90:93]
	v_mfma_f32_16x16x32_bf16 v[82:85], v[176:179], v[200:203], v[82:85]
	v_mfma_f32_16x16x32_bf16 v[74:77], v[168:171], v[208:211], v[74:77]
	v_mfma_f32_16x16x32_bf16 v[66:69], v[176:179], v[208:211], v[66:69]
	v_mfma_f32_16x16x32_bf16 v[122:125], v[172:175], v[188:191], v[122:125]
	v_mfma_f32_16x16x32_bf16 v[114:117], v[180:183], v[188:191], v[114:117]
	v_mfma_f32_16x16x32_bf16 v[106:109], v[172:175], v[196:199], v[106:109]
	v_mfma_f32_16x16x32_bf16 v[98:101], v[180:183], v[196:199], v[98:101]
	v_mfma_f32_16x16x32_bf16 v[90:93], v[172:175], v[204:207], v[90:93]
	v_mfma_f32_16x16x32_bf16 v[82:85], v[180:183], v[204:207], v[82:85]
	v_mfma_f32_16x16x32_bf16 v[74:77], v[172:175], v[212:215], v[74:77]
	v_mfma_f32_16x16x32_bf16 v[66:69], v[180:183], v[212:215], v[66:69]
	s_barrier
	s_add_i32 s26, s86, s35
	v_lshl_add_u64 v[224:225], v[216:217], 0, s[16:17]
	s_mov_b32 m0, s26
	ds_read_b128 v[184:187], v153 offset:49152
	ds_read_b128 v[188:191], v153 offset:50176
	ds_read_b128 v[192:195], v153 offset:51200
	ds_read_b128 v[196:199], v153 offset:52224
	ds_read_b128 v[200:203], v153 offset:53248
	ds_read_b128 v[204:207], v153 offset:54272
	ds_read_b128 v[208:211], v153 offset:55296
	ds_read_b128 v[212:215], v153 offset:56320
	global_load_lds_dwordx4 v[224:225], off
	v_lshl_add_u64 v[224:225], v[216:217], 0, s[18:19]
	s_add_i32 m0, s26, 0x2000
	s_add_i32 s26, s87, s35
	global_load_lds_dwordx4 v[224:225], off
	v_lshl_add_u64 v[224:225], v[216:217], 0, s[22:23]
	s_mov_b32 m0, s26
	v_lshl_add_u64 v[216:217], v[216:217], 0, s[24:25]
	global_load_lds_dwordx4 v[224:225], off
	s_add_i32 m0, s26, 0x2000
	s_nop 0
	global_load_lds_dwordx4 v[216:217], off
	v_lshl_add_u64 v[216:217], v[220:221], 0, s[20:21]
	s_mov_b32 m0, s70
	s_nop 0
	global_load_lds_dwordx4 v[216:217], off
	v_lshl_add_u64 v[216:217], v[222:223], 0, s[20:21]
	s_mov_b32 m0, s71
	s_nop 0
	global_load_lds_dwordx4 v[216:217], off
	s_waitcnt vmcnt(8)
	s_waitcnt lgkmcnt(0)
	s_barrier
	v_mfma_f32_16x16x32_bf16 v[62:65], v[144:147], v[184:187], v[62:65]
	v_mfma_f32_16x16x32_bf16 v[54:57], v[160:163], v[184:187], v[54:57]
	v_mfma_f32_16x16x32_bf16 v[46:49], v[144:147], v[192:195], v[46:49]
	v_mfma_f32_16x16x32_bf16 v[38:41], v[160:163], v[192:195], v[38:41]
	v_mfma_f32_16x16x32_bf16 v[30:33], v[144:147], v[200:203], v[30:33]
	v_mfma_f32_16x16x32_bf16 v[22:25], v[160:163], v[200:203], v[22:25]
	v_mfma_f32_16x16x32_bf16 v[14:17], v[144:147], v[208:211], v[14:17]
	v_mfma_f32_16x16x32_bf16 v[6:9], v[160:163], v[208:211], v[6:9]
	v_mfma_f32_16x16x32_bf16 v[62:65], v[156:159], v[188:191], v[62:65]
	v_mfma_f32_16x16x32_bf16 v[54:57], v[164:167], v[188:191], v[54:57]
	v_mfma_f32_16x16x32_bf16 v[46:49], v[156:159], v[196:199], v[46:49]
	v_mfma_f32_16x16x32_bf16 v[38:41], v[164:167], v[196:199], v[38:41]
	v_mfma_f32_16x16x32_bf16 v[30:33], v[156:159], v[204:207], v[30:33]
	v_mfma_f32_16x16x32_bf16 v[22:25], v[164:167], v[204:207], v[22:25]
	v_mfma_f32_16x16x32_bf16 v[14:17], v[156:159], v[212:215], v[14:17]
	v_mfma_f32_16x16x32_bf16 v[6:9], v[164:167], v[212:215], v[6:9]
	v_mfma_f32_16x16x32_bf16 v[58:61], v[168:171], v[184:187], v[58:61]
	v_mfma_f32_16x16x32_bf16 v[50:53], v[176:179], v[184:187], v[50:53]
	v_mfma_f32_16x16x32_bf16 v[42:45], v[168:171], v[192:195], v[42:45]
	v_mfma_f32_16x16x32_bf16 v[34:37], v[176:179], v[192:195], v[34:37]
	v_mfma_f32_16x16x32_bf16 v[26:29], v[168:171], v[200:203], v[26:29]
	v_mfma_f32_16x16x32_bf16 v[18:21], v[176:179], v[200:203], v[18:21]
	v_mfma_f32_16x16x32_bf16 v[10:13], v[168:171], v[208:211], v[10:13]
	v_mfma_f32_16x16x32_bf16 v[2:5], v[176:179], v[208:211], v[2:5]
	v_mfma_f32_16x16x32_bf16 v[58:61], v[172:175], v[188:191], v[58:61]
	v_mfma_f32_16x16x32_bf16 v[50:53], v[180:183], v[188:191], v[50:53]
	v_mfma_f32_16x16x32_bf16 v[42:45], v[172:175], v[196:199], v[42:45]
	v_mfma_f32_16x16x32_bf16 v[34:37], v[180:183], v[196:199], v[34:37]
	v_mfma_f32_16x16x32_bf16 v[26:29], v[172:175], v[204:207], v[26:29]
	v_mfma_f32_16x16x32_bf16 v[18:21], v[180:183], v[204:207], v[18:21]
	v_mfma_f32_16x16x32_bf16 v[10:13], v[172:175], v[212:215], v[10:13]
	v_mfma_f32_16x16x32_bf16 v[2:5], v[180:183], v[212:215], v[2:5]
	s_barrier
	s_add_i32 s85, s85, 2
	s_add_u32 s83, s83, 0x10000
	s_addc_u32 s84, s84, 0
	s_add_u32 s62, s62, 0x100
	s_addc_u32 s63, s63, 0
	s_cmp_gt_u32 s85, 29
	s_cbranch_scc0 .LBB0_783
	s_and_b64 vcc, exec, s[40:41]
	s_cbranch_vccz .LBB0_786
	s_barrier
	s_setprio 3

.LBB0_846:
	s_setprio 0
	s_andn2_b64 vcc, exec, s[50:51]
	s_mov_b32 s71, s69
	s_mov_b32 s2, s70
	s_mov_b64 s[50:51], s[44:45]
	s_mov_b64 s[52:53], s[4:5]
	s_cbranch_vccz .LBB0_864

.LBB0_858:
	ds_read_b128 v[26:29], v185
	ds_read_b128 v[30:33], v185 offset:1024
	ds_read_b128 v[18:21], v185 offset:2048
	ds_read_b128 v[22:25], v185 offset:3072
	ds_read_b128 v[10:13], v186
	ds_read_b128 v[14:17], v186 offset:1024
	ds_read_b128 v[2:5], v186 offset:2048
	ds_read_b128 v[6:9], v186 offset:3072
	s_add_u32 s26, s50, 0xfff50080
	s_addc_u32 s27, s51, -1
	s_cmp_eq_u32 s74, 40
	s_cselect_b32 s53, s5, s27
	s_cselect_b32 s52, s4, s26
	s_cselect_b32 s55, s45, s73
	s_cselect_b32 s54, s44, s72
	v_lshl_add_u64 v[176:177], s[50:51], 0, v[168:169]
	s_add_i32 m0, s59, 0xc000
	ds_read_b128 v[190:193], v187
	ds_read_b128 v[194:197], v187 offset:1024
	ds_read_b128 v[198:201], v187 offset:2048
	ds_read_b128 v[202:205], v187 offset:3072
	ds_read_b128 v[206:209], v187 offset:4096
	ds_read_b128 v[210:213], v187 offset:5120
	ds_read_b128 v[220:223], v187 offset:6144
	ds_read_b128 v[224:227], v187 offset:7168
	global_load_lds_dwordx4 v[176:177], off
	v_lshl_add_u64 v[176:177], s[50:51], 0, v[170:171]
	s_add_i32 m0, s59, 0xe000
	s_nop 0
	global_load_lds_dwordx4 v[176:177], off
	s_waitcnt vmcnt(8)
	s_waitcnt lgkmcnt(0)
	s_barrier
	v_mfma_scale_f32_16x16x128_f8f6f4 v[158:161], v[26:33], v[190:197], v[158:161], v188, v189 op_sel_hi:[0,0,0]
	v_mfma_scale_f32_16x16x128_f8f6f4 v[154:157], v[18:25], v[190:197], v[154:157], v188, v189 op_sel_hi:[0,0,0]
	v_mfma_scale_f32_16x16x128_f8f6f4 v[150:153], v[26:33], v[198:205], v[150:153], v188, v189 op_sel_hi:[0,0,0]
	v_mfma_scale_f32_16x16x128_f8f6f4 v[146:149], v[18:25], v[198:205], v[146:149], v188, v189 op_sel_hi:[0,0,0]
	v_mfma_scale_f32_16x16x128_f8f6f4 v[138:141], v[26:33], v[206:213], v[138:141], v188, v189 op_sel_hi:[0,0,0]
	v_mfma_scale_f32_16x16x128_f8f6f4 v[130:133], v[18:25], v[206:213], v[130:133], v188, v189 op_sel_hi:[0,0,0]
	v_mfma_scale_f32_16x16x128_f8f6f4 v[122:125], v[26:33], v[220:227], v[122:125], v188, v189 op_sel_hi:[0,0,0]
	v_mfma_scale_f32_16x16x128_f8f6f4 v[114:117], v[18:25], v[220:227], v[114:117], v188, v189 op_sel_hi:[0,0,0]
	v_mfma_scale_f32_16x16x128_f8f6f4 v[142:145], v[10:17], v[190:197], v[142:145], v188, v189 op_sel_hi:[0,0,0]
	v_mfma_scale_f32_16x16x128_f8f6f4 v[134:137], v[2:9], v[190:197], v[134:137], v188, v189 op_sel_hi:[0,0,0]
	v_mfma_scale_f32_16x16x128_f8f6f4 v[126:129], v[10:17], v[198:205], v[126:129], v188, v189 op_sel_hi:[0,0,0]
	v_mfma_scale_f32_16x16x128_f8f6f4 v[118:121], v[2:9], v[198:205], v[118:121], v188, v189 op_sel_hi:[0,0,0]
	v_mfma_scale_f32_16x16x128_f8f6f4 v[110:113], v[10:17], v[206:213], v[110:113], v188, v189 op_sel_hi:[0,0,0]
	v_mfma_scale_f32_16x16x128_f8f6f4 v[106:109], v[2:9], v[206:213], v[106:109], v188, v189 op_sel_hi:[0,0,0]
	v_mfma_scale_f32_16x16x128_f8f6f4 v[102:105], v[10:17], v[220:227], v[102:105], v188, v189 op_sel_hi:[0,0,0]
	v_mfma_scale_f32_16x16x128_f8f6f4 v[98:101], v[2:9], v[220:227], v[98:101], v188, v189 op_sel_hi:[0,0,0]
	s_barrier
	s_add_i32 s26, s67, s57
	v_lshl_add_u64 v[176:177], s[54:55], 0, v[162:163]
	s_mov_b32 m0, s26
	ds_read_b128 v[190:193], v187 offset:16384
	ds_read_b128 v[194:197], v187 offset:17408
	ds_read_b128 v[198:201], v187 offset:18432
	ds_read_b128 v[202:205], v187 offset:19456
	ds_read_b128 v[206:209], v187 offset:20480
	ds_read_b128 v[210:213], v187 offset:21504
	ds_read_b128 v[220:223], v187 offset:22528
	ds_read_b128 v[224:227], v187 offset:23552
	global_load_lds_dwordx4 v[176:177], off
	v_lshl_add_u64 v[178:179], v[176:177], 0, s[8:9]
	s_add_i32 m0, s26, 0x2000
	s_add_i32 s26, s68, s57
	global_load_lds_dwordx4 v[178:179], off
	v_lshl_add_u64 v[178:179], v[176:177], 0, s[10:11]
	s_mov_b32 m0, s26
	v_lshl_add_u64 v[180:181], s[52:53], 0, v[166:167]
	global_load_lds_dwordx4 v[178:179], off
	v_lshl_add_u64 v[178:179], v[176:177], 0, s[12:13]
	s_add_i32 m0, s26, 0x2000
	s_nop 0
	global_load_lds_dwordx4 v[178:179], off
	v_lshl_add_u64 v[178:179], s[52:53], 0, v[164:165]
	s_mov_b32 m0, s59
	s_nop 0
	global_load_lds_dwordx4 v[178:179], off
	s_mov_b32 m0, s60
	s_nop 0
	global_load_lds_dwordx4 v[180:181], off
	s_waitcnt vmcnt(8)
	s_waitcnt lgkmcnt(0)
	s_barrier
	v_mfma_scale_f32_16x16x128_f8f6f4 v[94:97], v[26:33], v[190:197], v[94:97], v188, v189 op_sel_hi:[0,0,0]
	v_mfma_scale_f32_16x16x128_f8f6f4 v[90:93], v[18:25], v[190:197], v[90:93], v188, v189 op_sel_hi:[0,0,0]
	v_mfma_scale_f32_16x16x128_f8f6f4 v[86:89], v[26:33], v[198:205], v[86:89], v188, v189 op_sel_hi:[0,0,0]
	v_mfma_scale_f32_16x16x128_f8f6f4 v[78:81], v[18:25], v[198:205], v[78:81], v188, v189 op_sel_hi:[0,0,0]
	v_mfma_scale_f32_16x16x128_f8f6f4 v[70:73], v[26:33], v[206:213], v[70:73], v188, v189 op_sel_hi:[0,0,0]
	v_mfma_scale_f32_16x16x128_f8f6f4 v[62:65], v[18:25], v[206:213], v[62:65], v188, v189 op_sel_hi:[0,0,0]
	v_mfma_scale_f32_16x16x128_f8f6f4 v[54:57], v[26:33], v[220:227], v[54:57], v188, v189 op_sel_hi:[0,0,0]
	v_mfma_scale_f32_16x16x128_f8f6f4 v[46:49], v[18:25], v[220:227], v[46:49], v188, v189 op_sel_hi:[0,0,0]
	v_mfma_scale_f32_16x16x128_f8f6f4 v[82:85], v[10:17], v[190:197], v[82:85], v188, v189 op_sel_hi:[0,0,0]
	v_mfma_scale_f32_16x16x128_f8f6f4 v[74:77], v[2:9], v[190:197], v[74:77], v188, v189 op_sel_hi:[0,0,0]
	v_mfma_scale_f32_16x16x128_f8f6f4 v[66:69], v[10:17], v[198:205], v[66:69], v188, v189 op_sel_hi:[0,0,0]
	v_mfma_scale_f32_16x16x128_f8f6f4 v[58:61], v[2:9], v[198:205], v[58:61], v188, v189 op_sel_hi:[0,0,0]
	v_mfma_scale_f32_16x16x128_f8f6f4 v[50:53], v[10:17], v[206:213], v[50:53], v188, v189 op_sel_hi:[0,0,0]
	v_mfma_scale_f32_16x16x128_f8f6f4 v[42:45], v[2:9], v[206:213], v[42:45], v188, v189 op_sel_hi:[0,0,0]
	v_mfma_scale_f32_16x16x128_f8f6f4 v[38:41], v[10:17], v[220:227], v[38:41], v188, v189 op_sel_hi:[0,0,0]
	v_mfma_scale_f32_16x16x128_f8f6f4 v[34:37], v[2:9], v[220:227], v[34:37], v188, v189 op_sel_hi:[0,0,0]
	s_barrier
	s_add_i32 s54, 0, 0x18000
	s_add_i32 s55, 0, 0x1c000
	v_add_u32_e32 v14, s54, v183
	v_add_u32_e32 v30, s55, v183
	ds_read_b128 v[2:5], v14
	ds_read_b128 v[6:9], v14 offset:1024
	ds_read_b128 v[10:13], v14 offset:2048
	ds_read_b128 v[14:17], v14 offset:3072
	ds_read_b128 v[18:21], v30
	ds_read_b128 v[22:25], v30 offset:1024
	ds_read_b128 v[26:29], v30 offset:2048
	ds_read_b128 v[30:33], v30 offset:3072
	s_add_u32 s26, s52, 0xb0000
	s_addc_u32 s27, s53, 0
	s_mov_b32 m0, s61
	v_lshl_add_u64 v[214:215], s[26:27], 0, v[164:165]
	ds_read_b128 v[190:193], v187 offset:32768
	ds_read_b128 v[194:197], v187 offset:33792
	ds_read_b128 v[198:201], v187 offset:34816
	ds_read_b128 v[202:205], v187 offset:35840
	ds_read_b128 v[206:209], v187 offset:36864
	ds_read_b128 v[210:213], v187 offset:37888
	ds_read_b128 v[220:223], v187 offset:38912
	ds_read_b128 v[224:227], v187 offset:39936
	global_load_lds_dwordx4 v[214:215], off
	v_lshl_add_u64 v[214:215], s[26:27], 0, v[166:167]
	s_mov_b32 m0, s62
	s_nop 0
	global_load_lds_dwordx4 v[214:215], off
	s_waitcnt vmcnt(8)
	s_waitcnt lgkmcnt(0)
	s_barrier
	v_mfma_scale_f32_16x16x128_f8f6f4 v[158:161], v[2:9], v[190:197], v[158:161], v188, v189 op_sel_hi:[0,0,0]
	v_mfma_scale_f32_16x16x128_f8f6f4 v[154:157], v[10:17], v[190:197], v[154:157], v188, v189 op_sel_hi:[0,0,0]
	v_mfma_scale_f32_16x16x128_f8f6f4 v[150:153], v[2:9], v[198:205], v[150:153], v188, v189 op_sel_hi:[0,0,0]
	v_mfma_scale_f32_16x16x128_f8f6f4 v[146:149], v[10:17], v[198:205], v[146:149], v188, v189 op_sel_hi:[0,0,0]
	v_mfma_scale_f32_16x16x128_f8f6f4 v[138:141], v[2:9], v[206:213], v[138:141], v188, v189 op_sel_hi:[0,0,0]
	v_mfma_scale_f32_16x16x128_f8f6f4 v[130:133], v[10:17], v[206:213], v[130:133], v188, v189 op_sel_hi:[0,0,0]
	v_mfma_scale_f32_16x16x128_f8f6f4 v[122:125], v[2:9], v[220:227], v[122:125], v188, v189 op_sel_hi:[0,0,0]
	v_mfma_scale_f32_16x16x128_f8f6f4 v[114:117], v[10:17], v[220:227], v[114:117], v188, v189 op_sel_hi:[0,0,0]
	v_mfma_scale_f32_16x16x128_f8f6f4 v[142:145], v[18:25], v[190:197], v[142:145], v188, v189 op_sel_hi:[0,0,0]
	v_mfma_scale_f32_16x16x128_f8f6f4 v[134:137], v[26:33], v[190:197], v[134:137], v188, v189 op_sel_hi:[0,0,0]
	v_mfma_scale_f32_16x16x128_f8f6f4 v[126:129], v[18:25], v[198:205], v[126:129], v188, v189 op_sel_hi:[0,0,0]
	v_mfma_scale_f32_16x16x128_f8f6f4 v[118:121], v[26:33], v[198:205], v[118:121], v188, v189 op_sel_hi:[0,0,0]
	v_mfma_scale_f32_16x16x128_f8f6f4 v[110:113], v[18:25], v[206:213], v[110:113], v188, v189 op_sel_hi:[0,0,0]
	v_mfma_scale_f32_16x16x128_f8f6f4 v[106:109], v[26:33], v[206:213], v[106:109], v188, v189 op_sel_hi:[0,0,0]
	v_mfma_scale_f32_16x16x128_f8f6f4 v[102:105], v[18:25], v[220:227], v[102:105], v188, v189 op_sel_hi:[0,0,0]
	v_mfma_scale_f32_16x16x128_f8f6f4 v[98:101], v[26:33], v[220:227], v[98:101], v188, v189 op_sel_hi:[0,0,0]
	s_barrier
	s_add_i32 s26, s54, s57
	v_lshl_add_u64 v[214:215], v[176:177], 0, s[16:17]
	s_mov_b32 m0, s26
	ds_read_b128 v[190:193], v187 offset:49152
	ds_read_b128 v[194:197], v187 offset:50176
	ds_read_b128 v[198:201], v187 offset:51200
	ds_read_b128 v[202:205], v187 offset:52224
	ds_read_b128 v[206:209], v187 offset:53248
	ds_read_b128 v[210:213], v187 offset:54272
	ds_read_b128 v[220:223], v187 offset:55296
	ds_read_b128 v[224:227], v187 offset:56320
	global_load_lds_dwordx4 v[214:215], off
	v_lshl_add_u64 v[214:215], v[176:177], 0, s[18:19]
	s_add_i32 m0, s26, 0x2000
	s_add_i32 s26, s55, s57
	global_load_lds_dwordx4 v[214:215], off
	v_lshl_add_u64 v[214:215], v[176:177], 0, s[22:23]
	s_mov_b32 m0, s26
	v_lshl_add_u64 v[176:177], v[176:177], 0, s[24:25]
	global_load_lds_dwordx4 v[214:215], off
	s_add_i32 m0, s26, 0x2000
	s_nop 0
	global_load_lds_dwordx4 v[176:177], off
	v_lshl_add_u64 v[176:177], v[178:179], 0, s[20:21]
	s_mov_b32 m0, s64
	s_nop 0
	global_load_lds_dwordx4 v[176:177], off
	v_lshl_add_u64 v[176:177], v[180:181], 0, s[20:21]
	s_mov_b32 m0, s65
	s_nop 0
	global_load_lds_dwordx4 v[176:177], off
	s_waitcnt vmcnt(8)
	s_waitcnt lgkmcnt(0)
	s_barrier
	v_mfma_scale_f32_16x16x128_f8f6f4 v[94:97], v[2:9], v[190:197], v[94:97], v188, v189 op_sel_hi:[0,0,0]
	v_mfma_scale_f32_16x16x128_f8f6f4 v[90:93], v[10:17], v[190:197], v[90:93], v188, v189 op_sel_hi:[0,0,0]
	v_mfma_scale_f32_16x16x128_f8f6f4 v[86:89], v[2:9], v[198:205], v[86:89], v188, v189 op_sel_hi:[0,0,0]
	v_mfma_scale_f32_16x16x128_f8f6f4 v[78:81], v[10:17], v[198:205], v[78:81], v188, v189 op_sel_hi:[0,0,0]
	v_mfma_scale_f32_16x16x128_f8f6f4 v[70:73], v[2:9], v[206:213], v[70:73], v188, v189 op_sel_hi:[0,0,0]
	v_mfma_scale_f32_16x16x128_f8f6f4 v[62:65], v[10:17], v[206:213], v[62:65], v188, v189 op_sel_hi:[0,0,0]
	v_mfma_scale_f32_16x16x128_f8f6f4 v[54:57], v[2:9], v[220:227], v[54:57], v188, v189 op_sel_hi:[0,0,0]
	v_mfma_scale_f32_16x16x128_f8f6f4 v[46:49], v[10:17], v[220:227], v[46:49], v188, v189 op_sel_hi:[0,0,0]
	v_mfma_scale_f32_16x16x128_f8f6f4 v[82:85], v[18:25], v[190:197], v[82:85], v188, v189 op_sel_hi:[0,0,0]
	v_mfma_scale_f32_16x16x128_f8f6f4 v[74:77], v[26:33], v[190:197], v[74:77], v188, v189 op_sel_hi:[0,0,0]
	v_mfma_scale_f32_16x16x128_f8f6f4 v[66:69], v[18:25], v[198:205], v[66:69], v188, v189 op_sel_hi:[0,0,0]
	v_mfma_scale_f32_16x16x128_f8f6f4 v[58:61], v[26:33], v[198:205], v[58:61], v188, v189 op_sel_hi:[0,0,0]
	v_mfma_scale_f32_16x16x128_f8f6f4 v[50:53], v[18:25], v[206:213], v[50:53], v188, v189 op_sel_hi:[0,0,0]
	v_mfma_scale_f32_16x16x128_f8f6f4 v[42:45], v[26:33], v[206:213], v[42:45], v188, v189 op_sel_hi:[0,0,0]
	v_mfma_scale_f32_16x16x128_f8f6f4 v[38:41], v[18:25], v[220:227], v[38:41], v188, v189 op_sel_hi:[0,0,0]
	v_mfma_scale_f32_16x16x128_f8f6f4 v[34:37], v[26:33], v[220:227], v[34:37], v188, v189 op_sel_hi:[0,0,0]
	s_barrier
	s_add_i32 s74, s74, 2
	s_add_u32 s72, s72, 0x10000
	s_addc_u32 s73, s73, 0
	s_add_u32 s50, s50, 0x100
	s_addc_u32 s51, s51, 0
	s_cmp_gt_u32 s74, 41
	s_cbranch_scc0 .LBB0_858
	s_and_b64 vcc, exec, s[40:41]
	s_cbranch_vccz .LBB0_861
	s_barrier
	s_setprio 3

.LBB0_977:
	s_setprio 0
	s_andn2_b64 vcc, exec, s[0:1]
	s_mov_b32 s2, s40
	s_mov_b32 s54, s44
	s_mov_b64 s[56:57], s[52:53]
	s_mov_b64 s[58:59], s[50:51]
	s_cbranch_vccz .LBB0_991

.LBB0_985:
	ds_read_b128 v[26:29], v185
	ds_read_b128 v[30:33], v185 offset:1024
	ds_read_b128 v[18:21], v185 offset:2048
	ds_read_b128 v[22:25], v185 offset:3072
	ds_read_b128 v[10:13], v186
	ds_read_b128 v[14:17], v186 offset:1024
	ds_read_b128 v[2:5], v186 offset:2048
	ds_read_b128 v[6:9], v186 offset:3072
	s_add_u32 s26, s56, 0xfffc0080
	s_addc_u32 s27, s57, -1
	s_cmp_eq_u32 s80, 12
	s_cselect_b32 s59, s45, s27
	s_cselect_b32 s58, s72, s26
	s_cselect_b32 s61, s41, s75
	s_cselect_b32 s60, s73, s74
	v_lshl_add_u64 v[176:177], s[56:57], 0, v[168:169]
	s_add_i32 m0, s55, 0xc000
	ds_read_b128 v[192:195], v187
	ds_read_b128 v[196:199], v187 offset:1024
	ds_read_b128 v[200:203], v187 offset:2048
	ds_read_b128 v[204:207], v187 offset:3072
	ds_read_b128 v[208:211], v187 offset:4096
	ds_read_b128 v[212:215], v187 offset:5120
	ds_read_b128 v[220:223], v187 offset:6144
	ds_read_b128 v[224:227], v187 offset:7168
	global_load_lds_dwordx4 v[176:177], off
	v_lshl_add_u64 v[176:177], s[56:57], 0, v[170:171]
	s_add_i32 m0, s55, 0xe000
	s_nop 0
	global_load_lds_dwordx4 v[176:177], off
	s_waitcnt vmcnt(8)
	s_waitcnt lgkmcnt(0)
	s_barrier
	v_mfma_scale_f32_16x16x128_f8f6f4 v[158:161], v[26:33], v[192:199], v[158:161], v188, v189 op_sel_hi:[0,0,0]
	v_mfma_scale_f32_16x16x128_f8f6f4 v[154:157], v[18:25], v[192:199], v[154:157], v188, v189 op_sel_hi:[0,0,0]
	v_mfma_scale_f32_16x16x128_f8f6f4 v[146:149], v[26:33], v[200:207], v[146:149], v188, v189 op_sel_hi:[0,0,0]
	v_mfma_scale_f32_16x16x128_f8f6f4 v[138:141], v[18:25], v[200:207], v[138:141], v188, v189 op_sel_hi:[0,0,0]
	v_mfma_scale_f32_16x16x128_f8f6f4 v[130:133], v[26:33], v[208:215], v[130:133], v188, v189 op_sel_hi:[0,0,0]
	v_mfma_scale_f32_16x16x128_f8f6f4 v[122:125], v[18:25], v[208:215], v[122:125], v188, v189 op_sel_hi:[0,0,0]
	v_mfma_scale_f32_16x16x128_f8f6f4 v[114:117], v[26:33], v[220:227], v[114:117], v188, v189 op_sel_hi:[0,0,0]
	v_mfma_scale_f32_16x16x128_f8f6f4 v[106:109], v[18:25], v[220:227], v[106:109], v188, v189 op_sel_hi:[0,0,0]
	v_mfma_scale_f32_16x16x128_f8f6f4 v[150:153], v[10:17], v[192:199], v[150:153], v188, v189 op_sel_hi:[0,0,0]
	v_mfma_scale_f32_16x16x128_f8f6f4 v[142:145], v[2:9], v[192:199], v[142:145], v188, v189 op_sel_hi:[0,0,0]
	v_mfma_scale_f32_16x16x128_f8f6f4 v[134:137], v[10:17], v[200:207], v[134:137], v188, v189 op_sel_hi:[0,0,0]
	v_mfma_scale_f32_16x16x128_f8f6f4 v[126:129], v[2:9], v[200:207], v[126:129], v188, v189 op_sel_hi:[0,0,0]
	v_mfma_scale_f32_16x16x128_f8f6f4 v[118:121], v[10:17], v[208:215], v[118:121], v188, v189 op_sel_hi:[0,0,0]
	v_mfma_scale_f32_16x16x128_f8f6f4 v[110:113], v[2:9], v[208:215], v[110:113], v188, v189 op_sel_hi:[0,0,0]
	v_mfma_scale_f32_16x16x128_f8f6f4 v[102:105], v[10:17], v[220:227], v[102:105], v188, v189 op_sel_hi:[0,0,0]
	v_mfma_scale_f32_16x16x128_f8f6f4 v[98:101], v[2:9], v[220:227], v[98:101], v188, v189 op_sel_hi:[0,0,0]
	s_barrier
	s_add_i32 s26, s70, s35
	v_lshl_add_u64 v[176:177], s[60:61], 0, v[162:163]
	s_mov_b32 m0, s26
	ds_read_b128 v[192:195], v187 offset:16384
	ds_read_b128 v[196:199], v187 offset:17408
	ds_read_b128 v[200:203], v187 offset:18432
	ds_read_b128 v[204:207], v187 offset:19456
	ds_read_b128 v[208:211], v187 offset:20480
	ds_read_b128 v[212:215], v187 offset:21504
	ds_read_b128 v[220:223], v187 offset:22528
	ds_read_b128 v[224:227], v187 offset:23552
	global_load_lds_dwordx4 v[176:177], off
	v_lshl_add_u64 v[178:179], v[176:177], 0, s[6:7]
	s_add_i32 m0, s26, 0x2000
	s_add_i32 s26, s71, s35
	global_load_lds_dwordx4 v[178:179], off
	v_lshl_add_u64 v[178:179], v[176:177], 0, s[8:9]
	s_mov_b32 m0, s26
	v_lshl_add_u64 v[180:181], s[58:59], 0, v[166:167]
	global_load_lds_dwordx4 v[178:179], off
	v_lshl_add_u64 v[178:179], v[176:177], 0, s[10:11]
	s_add_i32 m0, s26, 0x2000
	s_nop 0
	global_load_lds_dwordx4 v[178:179], off
	v_lshl_add_u64 v[178:179], s[58:59], 0, v[164:165]
	s_mov_b32 m0, s55
	s_nop 0
	global_load_lds_dwordx4 v[178:179], off
	s_mov_b32 m0, s63
	s_nop 0
	global_load_lds_dwordx4 v[180:181], off
	s_waitcnt vmcnt(8)
	s_waitcnt lgkmcnt(0)
	s_barrier
	v_mfma_scale_f32_16x16x128_f8f6f4 v[94:97], v[26:33], v[192:199], v[94:97], v188, v189 op_sel_hi:[0,0,0]
	v_mfma_scale_f32_16x16x128_f8f6f4 v[90:93], v[18:25], v[192:199], v[90:93], v188, v189 op_sel_hi:[0,0,0]
	v_mfma_scale_f32_16x16x128_f8f6f4 v[82:85], v[26:33], v[200:207], v[82:85], v188, v189 op_sel_hi:[0,0,0]
	v_mfma_scale_f32_16x16x128_f8f6f4 v[74:77], v[18:25], v[200:207], v[74:77], v188, v189 op_sel_hi:[0,0,0]
	v_mfma_scale_f32_16x16x128_f8f6f4 v[66:69], v[26:33], v[208:215], v[66:69], v188, v189 op_sel_hi:[0,0,0]
	v_mfma_scale_f32_16x16x128_f8f6f4 v[58:61], v[18:25], v[208:215], v[58:61], v188, v189 op_sel_hi:[0,0,0]
	v_mfma_scale_f32_16x16x128_f8f6f4 v[50:53], v[26:33], v[220:227], v[50:53], v188, v189 op_sel_hi:[0,0,0]
	v_mfma_scale_f32_16x16x128_f8f6f4 v[42:45], v[18:25], v[220:227], v[42:45], v188, v189 op_sel_hi:[0,0,0]
	v_mfma_scale_f32_16x16x128_f8f6f4 v[86:89], v[10:17], v[192:199], v[86:89], v188, v189 op_sel_hi:[0,0,0]
	v_mfma_scale_f32_16x16x128_f8f6f4 v[78:81], v[2:9], v[192:199], v[78:81], v188, v189 op_sel_hi:[0,0,0]
	v_mfma_scale_f32_16x16x128_f8f6f4 v[70:73], v[10:17], v[200:207], v[70:73], v188, v189 op_sel_hi:[0,0,0]
	v_mfma_scale_f32_16x16x128_f8f6f4 v[62:65], v[2:9], v[200:207], v[62:65], v188, v189 op_sel_hi:[0,0,0]
	v_mfma_scale_f32_16x16x128_f8f6f4 v[54:57], v[10:17], v[208:215], v[54:57], v188, v189 op_sel_hi:[0,0,0]
	v_mfma_scale_f32_16x16x128_f8f6f4 v[46:49], v[2:9], v[208:215], v[46:49], v188, v189 op_sel_hi:[0,0,0]
	v_mfma_scale_f32_16x16x128_f8f6f4 v[38:41], v[10:17], v[220:227], v[38:41], v188, v189 op_sel_hi:[0,0,0]
	v_mfma_scale_f32_16x16x128_f8f6f4 v[34:37], v[2:9], v[220:227], v[34:37], v188, v189 op_sel_hi:[0,0,0]
	s_barrier
	s_add_i32 s60, 0, 0x18000
	s_add_i32 s61, 0, 0x1c000
	v_add_u32_e32 v14, s60, v183
	v_add_u32_e32 v30, s61, v183
	ds_read_b128 v[2:5], v14
	ds_read_b128 v[6:9], v14 offset:1024
	ds_read_b128 v[10:13], v14 offset:2048
	ds_read_b128 v[14:17], v14 offset:3072
	ds_read_b128 v[18:21], v30
	ds_read_b128 v[22:25], v30 offset:1024
	ds_read_b128 v[26:29], v30 offset:2048
	ds_read_b128 v[30:33], v30 offset:3072
	s_add_u32 s26, s58, 0x40000
	s_addc_u32 s27, s59, 0
	s_mov_b32 m0, s64
	v_lshl_add_u64 v[216:217], s[26:27], 0, v[164:165]
	ds_read_b128 v[192:195], v187 offset:32768
	ds_read_b128 v[196:199], v187 offset:33792
	ds_read_b128 v[200:203], v187 offset:34816
	ds_read_b128 v[204:207], v187 offset:35840
	ds_read_b128 v[208:211], v187 offset:36864
	ds_read_b128 v[212:215], v187 offset:37888
	ds_read_b128 v[220:223], v187 offset:38912
	ds_read_b128 v[224:227], v187 offset:39936
	global_load_lds_dwordx4 v[216:217], off
	v_lshl_add_u64 v[216:217], s[26:27], 0, v[166:167]
	s_mov_b32 m0, s65
	s_nop 0
	global_load_lds_dwordx4 v[216:217], off
	s_waitcnt vmcnt(8)
	s_waitcnt lgkmcnt(0)
	s_barrier
	v_mfma_scale_f32_16x16x128_f8f6f4 v[158:161], v[2:9], v[192:199], v[158:161], v188, v189 op_sel_hi:[0,0,0]
	v_mfma_scale_f32_16x16x128_f8f6f4 v[154:157], v[10:17], v[192:199], v[154:157], v188, v189 op_sel_hi:[0,0,0]
	v_mfma_scale_f32_16x16x128_f8f6f4 v[146:149], v[2:9], v[200:207], v[146:149], v188, v189 op_sel_hi:[0,0,0]
	v_mfma_scale_f32_16x16x128_f8f6f4 v[138:141], v[10:17], v[200:207], v[138:141], v188, v189 op_sel_hi:[0,0,0]
	v_mfma_scale_f32_16x16x128_f8f6f4 v[130:133], v[2:9], v[208:215], v[130:133], v188, v189 op_sel_hi:[0,0,0]
	v_mfma_scale_f32_16x16x128_f8f6f4 v[122:125], v[10:17], v[208:215], v[122:125], v188, v189 op_sel_hi:[0,0,0]
	v_mfma_scale_f32_16x16x128_f8f6f4 v[114:117], v[2:9], v[220:227], v[114:117], v188, v189 op_sel_hi:[0,0,0]
	v_mfma_scale_f32_16x16x128_f8f6f4 v[106:109], v[10:17], v[220:227], v[106:109], v188, v189 op_sel_hi:[0,0,0]
	v_mfma_scale_f32_16x16x128_f8f6f4 v[150:153], v[18:25], v[192:199], v[150:153], v188, v189 op_sel_hi:[0,0,0]
	v_mfma_scale_f32_16x16x128_f8f6f4 v[142:145], v[26:33], v[192:199], v[142:145], v188, v189 op_sel_hi:[0,0,0]
	v_mfma_scale_f32_16x16x128_f8f6f4 v[134:137], v[18:25], v[200:207], v[134:137], v188, v189 op_sel_hi:[0,0,0]
	v_mfma_scale_f32_16x16x128_f8f6f4 v[126:129], v[26:33], v[200:207], v[126:129], v188, v189 op_sel_hi:[0,0,0]
	v_mfma_scale_f32_16x16x128_f8f6f4 v[118:121], v[18:25], v[208:215], v[118:121], v188, v189 op_sel_hi:[0,0,0]
	v_mfma_scale_f32_16x16x128_f8f6f4 v[110:113], v[26:33], v[208:215], v[110:113], v188, v189 op_sel_hi:[0,0,0]
	v_mfma_scale_f32_16x16x128_f8f6f4 v[102:105], v[18:25], v[220:227], v[102:105], v188, v189 op_sel_hi:[0,0,0]
	v_mfma_scale_f32_16x16x128_f8f6f4 v[98:101], v[26:33], v[220:227], v[98:101], v188, v189 op_sel_hi:[0,0,0]
	s_barrier
	s_add_i32 s26, s60, s35
	v_lshl_add_u64 v[216:217], v[176:177], 0, s[14:15]
	s_mov_b32 m0, s26
	ds_read_b128 v[192:195], v187 offset:49152
	ds_read_b128 v[196:199], v187 offset:50176
	ds_read_b128 v[200:203], v187 offset:51200
	ds_read_b128 v[204:207], v187 offset:52224
	ds_read_b128 v[208:211], v187 offset:53248
	ds_read_b128 v[212:215], v187 offset:54272
	ds_read_b128 v[220:223], v187 offset:55296
	ds_read_b128 v[224:227], v187 offset:56320
	global_load_lds_dwordx4 v[216:217], off
	v_lshl_add_u64 v[216:217], v[176:177], 0, s[16:17]
	s_add_i32 m0, s26, 0x2000
	s_add_i32 s26, s61, s35
	global_load_lds_dwordx4 v[216:217], off
	v_lshl_add_u64 v[216:217], v[176:177], 0, s[20:21]
	s_mov_b32 m0, s26
	v_lshl_add_u64 v[176:177], v[176:177], 0, s[22:23]
	global_load_lds_dwordx4 v[216:217], off
	s_add_i32 m0, s26, 0x2000
	s_nop 0
	global_load_lds_dwordx4 v[176:177], off
	v_lshl_add_u64 v[176:177], v[178:179], 0, s[18:19]
	s_mov_b32 m0, s67
	s_nop 0
	global_load_lds_dwordx4 v[176:177], off
	v_lshl_add_u64 v[176:177], v[180:181], 0, s[18:19]
	s_mov_b32 m0, s68
	s_nop 0
	global_load_lds_dwordx4 v[176:177], off
	s_waitcnt vmcnt(8)
	s_waitcnt lgkmcnt(0)
	s_barrier
	v_mfma_scale_f32_16x16x128_f8f6f4 v[94:97], v[2:9], v[192:199], v[94:97], v188, v189 op_sel_hi:[0,0,0]
	v_mfma_scale_f32_16x16x128_f8f6f4 v[90:93], v[10:17], v[192:199], v[90:93], v188, v189 op_sel_hi:[0,0,0]
	v_mfma_scale_f32_16x16x128_f8f6f4 v[82:85], v[2:9], v[200:207], v[82:85], v188, v189 op_sel_hi:[0,0,0]
	v_mfma_scale_f32_16x16x128_f8f6f4 v[74:77], v[10:17], v[200:207], v[74:77], v188, v189 op_sel_hi:[0,0,0]
	v_mfma_scale_f32_16x16x128_f8f6f4 v[66:69], v[2:9], v[208:215], v[66:69], v188, v189 op_sel_hi:[0,0,0]
	v_mfma_scale_f32_16x16x128_f8f6f4 v[58:61], v[10:17], v[208:215], v[58:61], v188, v189 op_sel_hi:[0,0,0]
	v_mfma_scale_f32_16x16x128_f8f6f4 v[50:53], v[2:9], v[220:227], v[50:53], v188, v189 op_sel_hi:[0,0,0]
	v_mfma_scale_f32_16x16x128_f8f6f4 v[42:45], v[10:17], v[220:227], v[42:45], v188, v189 op_sel_hi:[0,0,0]
	v_mfma_scale_f32_16x16x128_f8f6f4 v[86:89], v[18:25], v[192:199], v[86:89], v188, v189 op_sel_hi:[0,0,0]
	v_mfma_scale_f32_16x16x128_f8f6f4 v[78:81], v[26:33], v[192:199], v[78:81], v188, v189 op_sel_hi:[0,0,0]
	v_mfma_scale_f32_16x16x128_f8f6f4 v[70:73], v[18:25], v[200:207], v[70:73], v188, v189 op_sel_hi:[0,0,0]
	v_mfma_scale_f32_16x16x128_f8f6f4 v[62:65], v[26:33], v[200:207], v[62:65], v188, v189 op_sel_hi:[0,0,0]
	v_mfma_scale_f32_16x16x128_f8f6f4 v[54:57], v[18:25], v[208:215], v[54:57], v188, v189 op_sel_hi:[0,0,0]
	v_mfma_scale_f32_16x16x128_f8f6f4 v[46:49], v[26:33], v[208:215], v[46:49], v188, v189 op_sel_hi:[0,0,0]
	v_mfma_scale_f32_16x16x128_f8f6f4 v[38:41], v[18:25], v[220:227], v[38:41], v188, v189 op_sel_hi:[0,0,0]
	v_mfma_scale_f32_16x16x128_f8f6f4 v[34:37], v[26:33], v[220:227], v[34:37], v188, v189 op_sel_hi:[0,0,0]
	s_barrier
	s_add_i32 s80, s80, 2
	s_add_u32 s74, s74, 0x10000
	s_addc_u32 s75, s75, 0
	s_add_u32 s56, s56, 0x100
	s_addc_u32 s57, s57, 0
	s_cmp_gt_u32 s80, 13
	s_cbranch_scc0 .LBB0_985
	s_and_b64 vcc, exec, s[24:25]
	s_cbranch_vccz .LBB0_988
	s_barrier
	s_setprio 3

.LBB0_1192:
	ds_read_b128 v[66:69], v199
	ds_read_b128 v[70:73], v199 offset:1024
	ds_read_b128 v[82:85], v199 offset:2048
	ds_read_b128 v[86:89], v199 offset:3072
	ds_read_b128 v[146:149], v200
	ds_read_b128 v[150:153], v200 offset:1024
	ds_read_b128 v[154:157], v200 offset:2048
	ds_read_b128 v[158:161], v200 offset:3072
	s_add_u32 s26, s56, 0xfffc0080
	s_addc_u32 s27, s57, -1
	s_cmp_eq_u32 s73, 12
	s_cselect_b32 s59, s45, s27
	s_cselect_b32 s58, s69, s26
	s_cselect_b32 s27, s41, s72
	s_cselect_b32 s26, s70, s71
	v_lshl_add_u64 v[214:215], s[56:57], 0, v[176:177]
	s_add_i32 m0, s55, 0xc000
	ds_read_b128 v[162:165], v201
	ds_read_b128 v[166:169], v201 offset:1024
	ds_read_b128 v[184:187], v201 offset:2048
	ds_read_b128 v[188:191], v201 offset:3072
	ds_read_b128 v[192:195], v201 offset:4096
	ds_read_b128 v[202:205], v201 offset:5120
	ds_read_b128 v[206:209], v201 offset:6144
	ds_read_b128 v[210:213], v201 offset:7168
	global_load_lds_dwordx4 v[214:215], off
	v_lshl_add_u64 v[214:215], s[56:57], 0, v[178:179]
	s_add_i32 m0, s55, 0xe000
	s_nop 0
	global_load_lds_dwordx4 v[214:215], off
	s_waitcnt vmcnt(8)
	s_waitcnt lgkmcnt(0)
	s_barrier
	v_mfma_f32_16x16x32_bf16 v[142:145], v[66:69], v[162:165], v[142:145]
	v_mfma_f32_16x16x32_bf16 v[138:141], v[82:85], v[162:165], v[138:141]
	v_mfma_f32_16x16x32_bf16 v[126:129], v[66:69], v[184:187], v[126:129]
	v_mfma_f32_16x16x32_bf16 v[122:125], v[82:85], v[184:187], v[122:125]
	v_mfma_f32_16x16x32_bf16 v[110:113], v[66:69], v[192:195], v[110:113]
	v_mfma_f32_16x16x32_bf16 v[106:109], v[82:85], v[192:195], v[106:109]
	v_mfma_f32_16x16x32_bf16 v[94:97], v[66:69], v[206:209], v[94:97]
	v_mfma_f32_16x16x32_bf16 v[90:93], v[82:85], v[206:209], v[90:93]
	v_mfma_f32_16x16x32_bf16 v[142:145], v[70:73], v[166:169], v[142:145]
	v_mfma_f32_16x16x32_bf16 v[138:141], v[86:89], v[166:169], v[138:141]
	v_mfma_f32_16x16x32_bf16 v[126:129], v[70:73], v[188:191], v[126:129]
	v_mfma_f32_16x16x32_bf16 v[122:125], v[86:89], v[188:191], v[122:125]
	v_mfma_f32_16x16x32_bf16 v[110:113], v[70:73], v[202:205], v[110:113]
	v_mfma_f32_16x16x32_bf16 v[106:109], v[86:89], v[202:205], v[106:109]
	v_mfma_f32_16x16x32_bf16 v[94:97], v[70:73], v[210:213], v[94:97]
	v_mfma_f32_16x16x32_bf16 v[90:93], v[86:89], v[210:213], v[90:93]
	v_mfma_f32_16x16x32_bf16 v[134:137], v[146:149], v[162:165], v[134:137]
	v_mfma_f32_16x16x32_bf16 v[130:133], v[154:157], v[162:165], v[130:133]
	v_mfma_f32_16x16x32_bf16 v[118:121], v[146:149], v[184:187], v[118:121]
	v_mfma_f32_16x16x32_bf16 v[114:117], v[154:157], v[184:187], v[114:117]
	v_mfma_f32_16x16x32_bf16 v[102:105], v[146:149], v[192:195], v[102:105]
	v_mfma_f32_16x16x32_bf16 v[98:101], v[154:157], v[192:195], v[98:101]
	v_mfma_f32_16x16x32_bf16 v[78:81], v[146:149], v[206:209], v[78:81]
	v_mfma_f32_16x16x32_bf16 v[74:77], v[154:157], v[206:209], v[74:77]
	v_mfma_f32_16x16x32_bf16 v[134:137], v[150:153], v[166:169], v[134:137]
	v_mfma_f32_16x16x32_bf16 v[130:133], v[158:161], v[166:169], v[130:133]
	v_mfma_f32_16x16x32_bf16 v[118:121], v[150:153], v[188:191], v[118:121]
	v_mfma_f32_16x16x32_bf16 v[114:117], v[158:161], v[188:191], v[114:117]
	v_mfma_f32_16x16x32_bf16 v[102:105], v[150:153], v[202:205], v[102:105]
	v_mfma_f32_16x16x32_bf16 v[98:101], v[158:161], v[202:205], v[98:101]
	v_mfma_f32_16x16x32_bf16 v[78:81], v[150:153], v[210:213], v[78:81]
	v_mfma_f32_16x16x32_bf16 v[74:77], v[158:161], v[210:213], v[74:77]
	s_barrier
	v_lshl_add_u64 v[214:215], s[26:27], 0, v[170:171]
	s_add_i32 s26, s67, s35
	s_mov_b32 m0, s26
	ds_read_b128 v[162:165], v201 offset:16384
	ds_read_b128 v[166:169], v201 offset:17408
	ds_read_b128 v[184:187], v201 offset:18432
	ds_read_b128 v[188:191], v201 offset:19456
	ds_read_b128 v[192:195], v201 offset:20480
	ds_read_b128 v[202:205], v201 offset:21504
	ds_read_b128 v[206:209], v201 offset:22528
	ds_read_b128 v[210:213], v201 offset:23552
	global_load_lds_dwordx4 v[214:215], off
	v_lshl_add_u64 v[216:217], v[214:215], 0, s[6:7]
	s_add_i32 m0, s26, 0x2000
	s_add_i32 s26, s68, s35
	global_load_lds_dwordx4 v[216:217], off
	v_lshl_add_u64 v[216:217], v[214:215], 0, s[10:11]
	s_mov_b32 m0, s26
	v_lshl_add_u64 v[220:221], s[58:59], 0, v[174:175]
	global_load_lds_dwordx4 v[216:217], off
	v_lshl_add_u64 v[216:217], v[214:215], 0, s[12:13]
	s_add_i32 m0, s26, 0x2000
	s_nop 0
	global_load_lds_dwordx4 v[216:217], off
	v_lshl_add_u64 v[216:217], s[58:59], 0, v[172:173]
	s_mov_b32 m0, s55
	s_nop 0
	global_load_lds_dwordx4 v[216:217], off
	s_mov_b32 m0, s60
	s_nop 0
	global_load_lds_dwordx4 v[220:221], off
	s_waitcnt vmcnt(8)
	s_waitcnt lgkmcnt(0)
	s_barrier
	v_mfma_f32_16x16x32_bf16 v[62:65], v[66:69], v[162:165], v[62:65]
	v_mfma_f32_16x16x32_bf16 v[58:61], v[82:85], v[162:165], v[58:61]
	v_mfma_f32_16x16x32_bf16 v[46:49], v[66:69], v[184:187], v[46:49]
	v_mfma_f32_16x16x32_bf16 v[42:45], v[82:85], v[184:187], v[42:45]
	v_mfma_f32_16x16x32_bf16 v[30:33], v[66:69], v[192:195], v[30:33]
	v_mfma_f32_16x16x32_bf16 v[26:29], v[82:85], v[192:195], v[26:29]
	v_mfma_f32_16x16x32_bf16 v[14:17], v[66:69], v[206:209], v[14:17]
	v_mfma_f32_16x16x32_bf16 v[10:13], v[82:85], v[206:209], v[10:13]
	v_mfma_f32_16x16x32_bf16 v[62:65], v[70:73], v[166:169], v[62:65]
	v_mfma_f32_16x16x32_bf16 v[58:61], v[86:89], v[166:169], v[58:61]
	v_mfma_f32_16x16x32_bf16 v[46:49], v[70:73], v[188:191], v[46:49]
	v_mfma_f32_16x16x32_bf16 v[42:45], v[86:89], v[188:191], v[42:45]
	v_mfma_f32_16x16x32_bf16 v[30:33], v[70:73], v[202:205], v[30:33]
	v_mfma_f32_16x16x32_bf16 v[26:29], v[86:89], v[202:205], v[26:29]
	v_mfma_f32_16x16x32_bf16 v[14:17], v[70:73], v[210:213], v[14:17]
	v_mfma_f32_16x16x32_bf16 v[10:13], v[86:89], v[210:213], v[10:13]
	v_mfma_f32_16x16x32_bf16 v[54:57], v[146:149], v[162:165], v[54:57]
	v_mfma_f32_16x16x32_bf16 v[50:53], v[154:157], v[162:165], v[50:53]
	v_mfma_f32_16x16x32_bf16 v[38:41], v[146:149], v[184:187], v[38:41]
	v_mfma_f32_16x16x32_bf16 v[34:37], v[154:157], v[184:187], v[34:37]
	v_mfma_f32_16x16x32_bf16 v[22:25], v[146:149], v[192:195], v[22:25]
	v_mfma_f32_16x16x32_bf16 v[18:21], v[154:157], v[192:195], v[18:21]
	v_mfma_f32_16x16x32_bf16 v[6:9], v[146:149], v[206:209], v[6:9]
	v_mfma_f32_16x16x32_bf16 v[2:5], v[154:157], v[206:209], v[2:5]
	v_mfma_f32_16x16x32_bf16 v[54:57], v[150:153], v[166:169], v[54:57]
	v_mfma_f32_16x16x32_bf16 v[50:53], v[158:161], v[166:169], v[50:53]
	v_mfma_f32_16x16x32_bf16 v[38:41], v[150:153], v[188:191], v[38:41]
	v_mfma_f32_16x16x32_bf16 v[34:37], v[158:161], v[188:191], v[34:37]
	v_mfma_f32_16x16x32_bf16 v[22:25], v[150:153], v[202:205], v[22:25]
	v_mfma_f32_16x16x32_bf16 v[18:21], v[158:161], v[202:205], v[18:21]
	v_mfma_f32_16x16x32_bf16 v[6:9], v[150:153], v[210:213], v[6:9]
	v_mfma_f32_16x16x32_bf16 v[2:5], v[158:161], v[210:213], v[2:5]
	s_barrier
	s_add_i32 s74, 0, 0x18000
	s_add_i32 s75, 0, 0x1c000
	v_add_u32_e32 v86, s74, v197
	v_add_u32_e32 v158, s75, v197
	ds_read_b128 v[66:69], v86
	ds_read_b128 v[70:73], v86 offset:1024
	ds_read_b128 v[82:85], v86 offset:2048
	ds_read_b128 v[86:89], v86 offset:3072
	ds_read_b128 v[146:149], v158
	ds_read_b128 v[150:153], v158 offset:1024
	ds_read_b128 v[154:157], v158 offset:2048
	ds_read_b128 v[158:161], v158 offset:3072
	s_add_u32 s26, s58, 0x40000
	s_addc_u32 s27, s59, 0
	s_mov_b32 m0, s61
	v_lshl_add_u64 v[222:223], s[26:27], 0, v[172:173]
	ds_read_b128 v[162:165], v201 offset:32768
	ds_read_b128 v[166:169], v201 offset:33792
	ds_read_b128 v[184:187], v201 offset:34816
	ds_read_b128 v[188:191], v201 offset:35840
	ds_read_b128 v[192:195], v201 offset:36864
	ds_read_b128 v[202:205], v201 offset:37888
	ds_read_b128 v[206:209], v201 offset:38912
	ds_read_b128 v[210:213], v201 offset:39936
	global_load_lds_dwordx4 v[222:223], off
	v_lshl_add_u64 v[222:223], s[26:27], 0, v[174:175]
	s_mov_b32 m0, s62
	s_nop 0
	global_load_lds_dwordx4 v[222:223], off
	s_waitcnt vmcnt(8)
	s_waitcnt lgkmcnt(0)
	s_barrier
	v_mfma_f32_16x16x32_bf16 v[142:145], v[66:69], v[162:165], v[142:145]
	v_mfma_f32_16x16x32_bf16 v[138:141], v[82:85], v[162:165], v[138:141]
	v_mfma_f32_16x16x32_bf16 v[126:129], v[66:69], v[184:187], v[126:129]
	v_mfma_f32_16x16x32_bf16 v[122:125], v[82:85], v[184:187], v[122:125]
	v_mfma_f32_16x16x32_bf16 v[110:113], v[66:69], v[192:195], v[110:113]
	v_mfma_f32_16x16x32_bf16 v[106:109], v[82:85], v[192:195], v[106:109]
	v_mfma_f32_16x16x32_bf16 v[94:97], v[66:69], v[206:209], v[94:97]
	v_mfma_f32_16x16x32_bf16 v[90:93], v[82:85], v[206:209], v[90:93]
	v_mfma_f32_16x16x32_bf16 v[142:145], v[70:73], v[166:169], v[142:145]
	v_mfma_f32_16x16x32_bf16 v[138:141], v[86:89], v[166:169], v[138:141]
	v_mfma_f32_16x16x32_bf16 v[126:129], v[70:73], v[188:191], v[126:129]
	v_mfma_f32_16x16x32_bf16 v[122:125], v[86:89], v[188:191], v[122:125]
	v_mfma_f32_16x16x32_bf16 v[110:113], v[70:73], v[202:205], v[110:113]
	v_mfma_f32_16x16x32_bf16 v[106:109], v[86:89], v[202:205], v[106:109]
	v_mfma_f32_16x16x32_bf16 v[94:97], v[70:73], v[210:213], v[94:97]
	v_mfma_f32_16x16x32_bf16 v[90:93], v[86:89], v[210:213], v[90:93]
	v_mfma_f32_16x16x32_bf16 v[134:137], v[146:149], v[162:165], v[134:137]
	v_mfma_f32_16x16x32_bf16 v[130:133], v[154:157], v[162:165], v[130:133]
	v_mfma_f32_16x16x32_bf16 v[118:121], v[146:149], v[184:187], v[118:121]
	v_mfma_f32_16x16x32_bf16 v[114:117], v[154:157], v[184:187], v[114:117]
	v_mfma_f32_16x16x32_bf16 v[102:105], v[146:149], v[192:195], v[102:105]
	v_mfma_f32_16x16x32_bf16 v[98:101], v[154:157], v[192:195], v[98:101]
	v_mfma_f32_16x16x32_bf16 v[78:81], v[146:149], v[206:209], v[78:81]
	v_mfma_f32_16x16x32_bf16 v[74:77], v[154:157], v[206:209], v[74:77]
	v_mfma_f32_16x16x32_bf16 v[134:137], v[150:153], v[166:169], v[134:137]
	v_mfma_f32_16x16x32_bf16 v[130:133], v[158:161], v[166:169], v[130:133]
	v_mfma_f32_16x16x32_bf16 v[118:121], v[150:153], v[188:191], v[118:121]
	v_mfma_f32_16x16x32_bf16 v[114:117], v[158:161], v[188:191], v[114:117]
	v_mfma_f32_16x16x32_bf16 v[102:105], v[150:153], v[202:205], v[102:105]
	v_mfma_f32_16x16x32_bf16 v[98:101], v[158:161], v[202:205], v[98:101]
	v_mfma_f32_16x16x32_bf16 v[78:81], v[150:153], v[210:213], v[78:81]
	v_mfma_f32_16x16x32_bf16 v[74:77], v[158:161], v[210:213], v[74:77]
	s_barrier
	s_add_i32 s26, s74, s35
	v_lshl_add_u64 v[222:223], v[214:215], 0, s[16:17]
	s_mov_b32 m0, s26
	ds_read_b128 v[162:165], v201 offset:49152
	ds_read_b128 v[166:169], v201 offset:50176
	ds_read_b128 v[184:187], v201 offset:51200
	ds_read_b128 v[188:191], v201 offset:52224
	ds_read_b128 v[192:195], v201 offset:53248
	ds_read_b128 v[202:205], v201 offset:54272
	ds_read_b128 v[206:209], v201 offset:55296
	ds_read_b128 v[210:213], v201 offset:56320
	global_load_lds_dwordx4 v[222:223], off
	v_lshl_add_u64 v[222:223], v[214:215], 0, s[18:19]
	s_add_i32 m0, s26, 0x2000
	s_add_i32 s26, s75, s35
	global_load_lds_dwordx4 v[222:223], off
	v_lshl_add_u64 v[222:223], v[214:215], 0, s[22:23]
	s_mov_b32 m0, s26
	v_lshl_add_u64 v[214:215], v[214:215], 0, s[24:25]
	global_load_lds_dwordx4 v[222:223], off
	s_add_i32 m0, s26, 0x2000
	s_nop 0
	global_load_lds_dwordx4 v[214:215], off
	v_lshl_add_u64 v[214:215], v[216:217], 0, s[20:21]
	s_mov_b32 m0, s64
	s_nop 0
	global_load_lds_dwordx4 v[214:215], off
	v_lshl_add_u64 v[214:215], v[220:221], 0, s[20:21]
	s_mov_b32 m0, s65
	s_nop 0
	global_load_lds_dwordx4 v[214:215], off
	s_waitcnt vmcnt(8)
	s_waitcnt lgkmcnt(0)
	s_barrier
	v_mfma_f32_16x16x32_bf16 v[62:65], v[66:69], v[162:165], v[62:65]
	v_mfma_f32_16x16x32_bf16 v[58:61], v[82:85], v[162:165], v[58:61]
	v_mfma_f32_16x16x32_bf16 v[46:49], v[66:69], v[184:187], v[46:49]
	v_mfma_f32_16x16x32_bf16 v[42:45], v[82:85], v[184:187], v[42:45]
	v_mfma_f32_16x16x32_bf16 v[30:33], v[66:69], v[192:195], v[30:33]
	v_mfma_f32_16x16x32_bf16 v[26:29], v[82:85], v[192:195], v[26:29]
	v_mfma_f32_16x16x32_bf16 v[14:17], v[66:69], v[206:209], v[14:17]
	v_mfma_f32_16x16x32_bf16 v[10:13], v[82:85], v[206:209], v[10:13]
	v_mfma_f32_16x16x32_bf16 v[62:65], v[70:73], v[166:169], v[62:65]
	v_mfma_f32_16x16x32_bf16 v[58:61], v[86:89], v[166:169], v[58:61]
	v_mfma_f32_16x16x32_bf16 v[46:49], v[70:73], v[188:191], v[46:49]
	v_mfma_f32_16x16x32_bf16 v[42:45], v[86:89], v[188:191], v[42:45]
	v_mfma_f32_16x16x32_bf16 v[30:33], v[70:73], v[202:205], v[30:33]
	v_mfma_f32_16x16x32_bf16 v[26:29], v[86:89], v[202:205], v[26:29]
	v_mfma_f32_16x16x32_bf16 v[14:17], v[70:73], v[210:213], v[14:17]
	v_mfma_f32_16x16x32_bf16 v[10:13], v[86:89], v[210:213], v[10:13]
	v_mfma_f32_16x16x32_bf16 v[54:57], v[146:149], v[162:165], v[54:57]
	v_mfma_f32_16x16x32_bf16 v[50:53], v[154:157], v[162:165], v[50:53]
	v_mfma_f32_16x16x32_bf16 v[38:41], v[146:149], v[184:187], v[38:41]
	v_mfma_f32_16x16x32_bf16 v[34:37], v[154:157], v[184:187], v[34:37]
	v_mfma_f32_16x16x32_bf16 v[22:25], v[146:149], v[192:195], v[22:25]
	v_mfma_f32_16x16x32_bf16 v[18:21], v[154:157], v[192:195], v[18:21]
	v_mfma_f32_16x16x32_bf16 v[6:9], v[146:149], v[206:209], v[6:9]
	v_mfma_f32_16x16x32_bf16 v[2:5], v[154:157], v[206:209], v[2:5]
	v_mfma_f32_16x16x32_bf16 v[54:57], v[150:153], v[166:169], v[54:57]
	v_mfma_f32_16x16x32_bf16 v[50:53], v[158:161], v[166:169], v[50:53]
	v_mfma_f32_16x16x32_bf16 v[38:41], v[150:153], v[188:191], v[38:41]
	v_mfma_f32_16x16x32_bf16 v[34:37], v[158:161], v[188:191], v[34:37]
	v_mfma_f32_16x16x32_bf16 v[22:25], v[150:153], v[202:205], v[22:25]
	v_mfma_f32_16x16x32_bf16 v[18:21], v[158:161], v[202:205], v[18:21]
	v_mfma_f32_16x16x32_bf16 v[6:9], v[150:153], v[210:213], v[6:9]
	v_mfma_f32_16x16x32_bf16 v[2:5], v[158:161], v[210:213], v[2:5]
	s_barrier
	s_add_i32 s73, s73, 2
	s_add_u32 s71, s71, 0x10000
	s_addc_u32 s72, s72, 0
	s_add_u32 s56, s56, 0x100
	s_addc_u32 s57, s57, 0
	s_cmp_gt_u32 s73, 13
	s_cbranch_scc0 .LBB0_1192
	s_and_b64 vcc, exec, s[36:37]
	s_cbranch_vccz .LBB0_1195
	s_barrier
	s_setprio 3

.LBB0_1263:
	s_setprio 0
	s_andn2_b64 vcc, exec, s[56:57]
	s_mov_b32 s2, s44
	s_mov_b32 s56, s50
	s_mov_b64 s[58:59], s[54:55]
	s_mov_b64 s[60:61], s[52:53]
	s_cbranch_vccz .LBB0_1277

.LBB0_1271:
	ds_read_b128 v[144:147], v158
	ds_read_b128 v[148:151], v158 offset:1024
	ds_read_b128 v[152:155], v158 offset:2048
	ds_read_b128 v[162:165], v158 offset:3072
	ds_read_b128 v[166:169], v159
	ds_read_b128 v[170:173], v159 offset:1024
	ds_read_b128 v[174:177], v159 offset:2048
	ds_read_b128 v[178:181], v159 offset:3072
	s_add_u32 s26, s58, 0xfff80080
	s_addc_u32 s27, s59, -1
	s_cmp_eq_u32 s80, 28
	s_cselect_b32 s61, s51, s27
	s_cselect_b32 s60, s57, s26
	s_cselect_b32 s27, s45, s75
	s_cselect_b32 s26, s73, s74
	v_lshl_add_u64 v[214:215], s[58:59], 0, v[136:137]
	s_add_i32 m0, s63, 0xc000
	ds_read_b128 v[182:185], v160
	ds_read_b128 v[186:189], v160 offset:1024
	ds_read_b128 v[190:193], v160 offset:2048
	ds_read_b128 v[194:197], v160 offset:3072
	ds_read_b128 v[198:201], v160 offset:4096
	ds_read_b128 v[202:205], v160 offset:5120
	ds_read_b128 v[206:209], v160 offset:6144
	ds_read_b128 v[210:213], v160 offset:7168
	global_load_lds_dwordx4 v[214:215], off
	v_lshl_add_u64 v[214:215], s[58:59], 0, v[138:139]
	s_add_i32 m0, s63, 0xe000
	s_nop 0
	global_load_lds_dwordx4 v[214:215], off
	s_waitcnt vmcnt(8)
	s_waitcnt lgkmcnt(0)
	s_barrier
	v_mfma_f32_16x16x32_bf16 v[126:129], v[144:147], v[182:185], v[126:129]
	v_mfma_f32_16x16x32_bf16 v[122:125], v[152:155], v[182:185], v[122:125]
	v_mfma_f32_16x16x32_bf16 v[118:121], v[144:147], v[190:193], v[118:121]
	v_mfma_f32_16x16x32_bf16 v[114:117], v[152:155], v[190:193], v[114:117]
	v_mfma_f32_16x16x32_bf16 v[106:109], v[144:147], v[198:201], v[106:109]
	v_mfma_f32_16x16x32_bf16 v[98:101], v[152:155], v[198:201], v[98:101]
	v_mfma_f32_16x16x32_bf16 v[90:93], v[144:147], v[206:209], v[90:93]
	v_mfma_f32_16x16x32_bf16 v[82:85], v[152:155], v[206:209], v[82:85]
	v_mfma_f32_16x16x32_bf16 v[126:129], v[148:151], v[186:189], v[126:129]
	v_mfma_f32_16x16x32_bf16 v[122:125], v[162:165], v[186:189], v[122:125]
	v_mfma_f32_16x16x32_bf16 v[118:121], v[148:151], v[194:197], v[118:121]
	v_mfma_f32_16x16x32_bf16 v[114:117], v[162:165], v[194:197], v[114:117]
	v_mfma_f32_16x16x32_bf16 v[106:109], v[148:151], v[202:205], v[106:109]
	v_mfma_f32_16x16x32_bf16 v[98:101], v[162:165], v[202:205], v[98:101]
	v_mfma_f32_16x16x32_bf16 v[90:93], v[148:151], v[210:213], v[90:93]
	v_mfma_f32_16x16x32_bf16 v[82:85], v[162:165], v[210:213], v[82:85]
	v_mfma_f32_16x16x32_bf16 v[110:113], v[166:169], v[182:185], v[110:113]
	v_mfma_f32_16x16x32_bf16 v[102:105], v[174:177], v[182:185], v[102:105]
	v_mfma_f32_16x16x32_bf16 v[94:97], v[166:169], v[190:193], v[94:97]
	v_mfma_f32_16x16x32_bf16 v[86:89], v[174:177], v[190:193], v[86:89]
	v_mfma_f32_16x16x32_bf16 v[78:81], v[166:169], v[198:201], v[78:81]
	v_mfma_f32_16x16x32_bf16 v[74:77], v[174:177], v[198:201], v[74:77]
	v_mfma_f32_16x16x32_bf16 v[70:73], v[166:169], v[206:209], v[70:73]
	v_mfma_f32_16x16x32_bf16 v[66:69], v[174:177], v[206:209], v[66:69]
	v_mfma_f32_16x16x32_bf16 v[110:113], v[170:173], v[186:189], v[110:113]
	v_mfma_f32_16x16x32_bf16 v[102:105], v[178:181], v[186:189], v[102:105]
	v_mfma_f32_16x16x32_bf16 v[94:97], v[170:173], v[194:197], v[94:97]
	v_mfma_f32_16x16x32_bf16 v[86:89], v[178:181], v[194:197], v[86:89]
	v_mfma_f32_16x16x32_bf16 v[78:81], v[170:173], v[202:205], v[78:81]
	v_mfma_f32_16x16x32_bf16 v[74:77], v[178:181], v[202:205], v[74:77]
	v_mfma_f32_16x16x32_bf16 v[70:73], v[170:173], v[210:213], v[70:73]
	v_mfma_f32_16x16x32_bf16 v[66:69], v[178:181], v[210:213], v[66:69]
	s_barrier
	v_lshl_add_u64 v[214:215], s[26:27], 0, v[130:131]
	s_add_i32 s26, s71, s35
	s_mov_b32 m0, s26
	ds_read_b128 v[182:185], v160 offset:16384
	ds_read_b128 v[186:189], v160 offset:17408
	ds_read_b128 v[190:193], v160 offset:18432
	ds_read_b128 v[194:197], v160 offset:19456
	ds_read_b128 v[198:201], v160 offset:20480
	ds_read_b128 v[202:205], v160 offset:21504
	ds_read_b128 v[206:209], v160 offset:22528
	ds_read_b128 v[210:213], v160 offset:23552
	global_load_lds_dwordx4 v[214:215], off
	v_lshl_add_u64 v[216:217], v[214:215], 0, s[6:7]
	s_add_i32 m0, s26, 0x2000
	s_add_i32 s26, s72, s35
	global_load_lds_dwordx4 v[216:217], off
	v_lshl_add_u64 v[216:217], v[214:215], 0, s[8:9]
	s_mov_b32 m0, s26
	v_lshl_add_u64 v[220:221], s[60:61], 0, v[134:135]
	global_load_lds_dwordx4 v[216:217], off
	v_lshl_add_u64 v[216:217], v[214:215], 0, s[10:11]
	s_add_i32 m0, s26, 0x2000
	s_nop 0
	global_load_lds_dwordx4 v[216:217], off
	v_lshl_add_u64 v[216:217], s[60:61], 0, v[132:133]
	s_mov_b32 m0, s63
	s_nop 0
	global_load_lds_dwordx4 v[216:217], off
	s_mov_b32 m0, s64
	s_nop 0
	global_load_lds_dwordx4 v[220:221], off
	s_waitcnt vmcnt(8)
	s_waitcnt lgkmcnt(0)
	s_barrier
	v_mfma_f32_16x16x32_bf16 v[62:65], v[144:147], v[182:185], v[62:65]
	v_mfma_f32_16x16x32_bf16 v[58:61], v[152:155], v[182:185], v[58:61]
	v_mfma_f32_16x16x32_bf16 v[54:57], v[144:147], v[190:193], v[54:57]
	v_mfma_f32_16x16x32_bf16 v[46:49], v[152:155], v[190:193], v[46:49]
	v_mfma_f32_16x16x32_bf16 v[38:41], v[144:147], v[198:201], v[38:41]
	v_mfma_f32_16x16x32_bf16 v[30:33], v[152:155], v[198:201], v[30:33]
	v_mfma_f32_16x16x32_bf16 v[22:25], v[144:147], v[206:209], v[22:25]
	v_mfma_f32_16x16x32_bf16 v[14:17], v[152:155], v[206:209], v[14:17]
	v_mfma_f32_16x16x32_bf16 v[62:65], v[148:151], v[186:189], v[62:65]
	v_mfma_f32_16x16x32_bf16 v[58:61], v[162:165], v[186:189], v[58:61]
	v_mfma_f32_16x16x32_bf16 v[54:57], v[148:151], v[194:197], v[54:57]
	v_mfma_f32_16x16x32_bf16 v[46:49], v[162:165], v[194:197], v[46:49]
	v_mfma_f32_16x16x32_bf16 v[38:41], v[148:151], v[202:205], v[38:41]
	v_mfma_f32_16x16x32_bf16 v[30:33], v[162:165], v[202:205], v[30:33]
	v_mfma_f32_16x16x32_bf16 v[22:25], v[148:151], v[210:213], v[22:25]
	v_mfma_f32_16x16x32_bf16 v[14:17], v[162:165], v[210:213], v[14:17]
	v_mfma_f32_16x16x32_bf16 v[50:53], v[166:169], v[182:185], v[50:53]
	v_mfma_f32_16x16x32_bf16 v[42:45], v[174:177], v[182:185], v[42:45]
	v_mfma_f32_16x16x32_bf16 v[34:37], v[166:169], v[190:193], v[34:37]
	v_mfma_f32_16x16x32_bf16 v[26:29], v[174:177], v[190:193], v[26:29]
	v_mfma_f32_16x16x32_bf16 v[18:21], v[166:169], v[198:201], v[18:21]
	v_mfma_f32_16x16x32_bf16 v[10:13], v[174:177], v[198:201], v[10:13]
	v_mfma_f32_16x16x32_bf16 v[6:9], v[166:169], v[206:209], v[6:9]
	v_mfma_f32_16x16x32_bf16 v[2:5], v[174:177], v[206:209], v[2:5]
	v_mfma_f32_16x16x32_bf16 v[50:53], v[170:173], v[186:189], v[50:53]
	v_mfma_f32_16x16x32_bf16 v[42:45], v[178:181], v[186:189], v[42:45]
	v_mfma_f32_16x16x32_bf16 v[34:37], v[170:173], v[194:197], v[34:37]
	v_mfma_f32_16x16x32_bf16 v[26:29], v[178:181], v[194:197], v[26:29]
	v_mfma_f32_16x16x32_bf16 v[18:21], v[170:173], v[202:205], v[18:21]
	v_mfma_f32_16x16x32_bf16 v[10:13], v[178:181], v[202:205], v[10:13]
	v_mfma_f32_16x16x32_bf16 v[6:9], v[170:173], v[210:213], v[6:9]
	v_mfma_f32_16x16x32_bf16 v[2:5], v[178:181], v[210:213], v[2:5]
	s_barrier
	s_add_i32 s81, 0, 0x18000
	v_add_u32_e32 v161, s81, v156
	s_add_i32 s82, 0, 0x1c000
	ds_read_b128 v[144:147], v161
	ds_read_b128 v[148:151], v161 offset:1024
	ds_read_b128 v[152:155], v161 offset:2048
	ds_read_b128 v[162:165], v161 offset:3072
	v_add_u32_e32 v161, s82, v156
	ds_read_b128 v[166:169], v161
	ds_read_b128 v[170:173], v161 offset:1024
	ds_read_b128 v[174:177], v161 offset:2048
	ds_read_b128 v[178:181], v161 offset:3072
	s_add_u32 s26, s60, 0x80000
	s_addc_u32 s27, s61, 0
	s_mov_b32 m0, s65
	v_lshl_add_u64 v[222:223], s[26:27], 0, v[132:133]
	ds_read_b128 v[182:185], v160 offset:32768
	ds_read_b128 v[186:189], v160 offset:33792
	ds_read_b128 v[190:193], v160 offset:34816
	ds_read_b128 v[194:197], v160 offset:35840
	ds_read_b128 v[198:201], v160 offset:36864
	ds_read_b128 v[202:205], v160 offset:37888
	ds_read_b128 v[206:209], v160 offset:38912
	ds_read_b128 v[210:213], v160 offset:39936
	global_load_lds_dwordx4 v[222:223], off
	v_lshl_add_u64 v[222:223], s[26:27], 0, v[134:135]
	s_mov_b32 m0, s66
	s_nop 0
	global_load_lds_dwordx4 v[222:223], off
	s_waitcnt vmcnt(8)
	s_waitcnt lgkmcnt(0)
	s_barrier
	v_mfma_f32_16x16x32_bf16 v[126:129], v[144:147], v[182:185], v[126:129]
	v_mfma_f32_16x16x32_bf16 v[122:125], v[152:155], v[182:185], v[122:125]
	v_mfma_f32_16x16x32_bf16 v[118:121], v[144:147], v[190:193], v[118:121]
	v_mfma_f32_16x16x32_bf16 v[114:117], v[152:155], v[190:193], v[114:117]
	v_mfma_f32_16x16x32_bf16 v[106:109], v[144:147], v[198:201], v[106:109]
	v_mfma_f32_16x16x32_bf16 v[98:101], v[152:155], v[198:201], v[98:101]
	v_mfma_f32_16x16x32_bf16 v[90:93], v[144:147], v[206:209], v[90:93]
	v_mfma_f32_16x16x32_bf16 v[82:85], v[152:155], v[206:209], v[82:85]
	v_mfma_f32_16x16x32_bf16 v[126:129], v[148:151], v[186:189], v[126:129]
	v_mfma_f32_16x16x32_bf16 v[122:125], v[162:165], v[186:189], v[122:125]
	v_mfma_f32_16x16x32_bf16 v[118:121], v[148:151], v[194:197], v[118:121]
	v_mfma_f32_16x16x32_bf16 v[114:117], v[162:165], v[194:197], v[114:117]
	v_mfma_f32_16x16x32_bf16 v[106:109], v[148:151], v[202:205], v[106:109]
	v_mfma_f32_16x16x32_bf16 v[98:101], v[162:165], v[202:205], v[98:101]
	v_mfma_f32_16x16x32_bf16 v[90:93], v[148:151], v[210:213], v[90:93]
	v_mfma_f32_16x16x32_bf16 v[82:85], v[162:165], v[210:213], v[82:85]
	v_mfma_f32_16x16x32_bf16 v[110:113], v[166:169], v[182:185], v[110:113]
	v_mfma_f32_16x16x32_bf16 v[102:105], v[174:177], v[182:185], v[102:105]
	v_mfma_f32_16x16x32_bf16 v[94:97], v[166:169], v[190:193], v[94:97]
	v_mfma_f32_16x16x32_bf16 v[86:89], v[174:177], v[190:193], v[86:89]
	v_mfma_f32_16x16x32_bf16 v[78:81], v[166:169], v[198:201], v[78:81]
	v_mfma_f32_16x16x32_bf16 v[74:77], v[174:177], v[198:201], v[74:77]
	v_mfma_f32_16x16x32_bf16 v[70:73], v[166:169], v[206:209], v[70:73]
	v_mfma_f32_16x16x32_bf16 v[66:69], v[174:177], v[206:209], v[66:69]
	v_mfma_f32_16x16x32_bf16 v[110:113], v[170:173], v[186:189], v[110:113]
	v_mfma_f32_16x16x32_bf16 v[102:105], v[178:181], v[186:189], v[102:105]
	v_mfma_f32_16x16x32_bf16 v[94:97], v[170:173], v[194:197], v[94:97]
	v_mfma_f32_16x16x32_bf16 v[86:89], v[178:181], v[194:197], v[86:89]
	v_mfma_f32_16x16x32_bf16 v[78:81], v[170:173], v[202:205], v[78:81]
	v_mfma_f32_16x16x32_bf16 v[74:77], v[178:181], v[202:205], v[74:77]
	v_mfma_f32_16x16x32_bf16 v[70:73], v[170:173], v[210:213], v[70:73]
	v_mfma_f32_16x16x32_bf16 v[66:69], v[178:181], v[210:213], v[66:69]
	s_barrier
	s_add_i32 s26, s81, s35
	v_lshl_add_u64 v[222:223], v[214:215], 0, s[14:15]
	s_mov_b32 m0, s26
	ds_read_b128 v[182:185], v160 offset:49152
	ds_read_b128 v[186:189], v160 offset:50176
	ds_read_b128 v[190:193], v160 offset:51200
	ds_read_b128 v[194:197], v160 offset:52224
	ds_read_b128 v[198:201], v160 offset:53248
	ds_read_b128 v[202:205], v160 offset:54272
	ds_read_b128 v[206:209], v160 offset:55296
	ds_read_b128 v[210:213], v160 offset:56320
	global_load_lds_dwordx4 v[222:223], off
	v_lshl_add_u64 v[222:223], v[214:215], 0, s[16:17]
	s_add_i32 m0, s26, 0x2000
	s_add_i32 s26, s82, s35
	global_load_lds_dwordx4 v[222:223], off
	v_lshl_add_u64 v[222:223], v[214:215], 0, s[20:21]
	s_mov_b32 m0, s26
	v_lshl_add_u64 v[214:215], v[214:215], 0, s[22:23]
	global_load_lds_dwordx4 v[222:223], off
	s_add_i32 m0, s26, 0x2000
	s_nop 0
	global_load_lds_dwordx4 v[214:215], off
	v_lshl_add_u64 v[214:215], v[216:217], 0, s[18:19]
	s_mov_b32 m0, s68
	s_nop 0
	global_load_lds_dwordx4 v[214:215], off
	v_lshl_add_u64 v[214:215], v[220:221], 0, s[18:19]
	s_mov_b32 m0, s69
	s_nop 0
	global_load_lds_dwordx4 v[214:215], off
	s_waitcnt vmcnt(8)
	s_waitcnt lgkmcnt(0)
	s_barrier
	v_mfma_f32_16x16x32_bf16 v[62:65], v[144:147], v[182:185], v[62:65]
	v_mfma_f32_16x16x32_bf16 v[58:61], v[152:155], v[182:185], v[58:61]
	v_mfma_f32_16x16x32_bf16 v[54:57], v[144:147], v[190:193], v[54:57]
	v_mfma_f32_16x16x32_bf16 v[46:49], v[152:155], v[190:193], v[46:49]
	v_mfma_f32_16x16x32_bf16 v[38:41], v[144:147], v[198:201], v[38:41]
	v_mfma_f32_16x16x32_bf16 v[30:33], v[152:155], v[198:201], v[30:33]
	v_mfma_f32_16x16x32_bf16 v[22:25], v[144:147], v[206:209], v[22:25]
	v_mfma_f32_16x16x32_bf16 v[14:17], v[152:155], v[206:209], v[14:17]
	v_mfma_f32_16x16x32_bf16 v[62:65], v[148:151], v[186:189], v[62:65]
	v_mfma_f32_16x16x32_bf16 v[58:61], v[162:165], v[186:189], v[58:61]
	v_mfma_f32_16x16x32_bf16 v[54:57], v[148:151], v[194:197], v[54:57]
	v_mfma_f32_16x16x32_bf16 v[46:49], v[162:165], v[194:197], v[46:49]
	v_mfma_f32_16x16x32_bf16 v[38:41], v[148:151], v[202:205], v[38:41]
	v_mfma_f32_16x16x32_bf16 v[30:33], v[162:165], v[202:205], v[30:33]
	v_mfma_f32_16x16x32_bf16 v[22:25], v[148:151], v[210:213], v[22:25]
	v_mfma_f32_16x16x32_bf16 v[14:17], v[162:165], v[210:213], v[14:17]
	v_mfma_f32_16x16x32_bf16 v[50:53], v[166:169], v[182:185], v[50:53]
	v_mfma_f32_16x16x32_bf16 v[42:45], v[174:177], v[182:185], v[42:45]
	v_mfma_f32_16x16x32_bf16 v[34:37], v[166:169], v[190:193], v[34:37]
	v_mfma_f32_16x16x32_bf16 v[26:29], v[174:177], v[190:193], v[26:29]
	v_mfma_f32_16x16x32_bf16 v[18:21], v[166:169], v[198:201], v[18:21]
	v_mfma_f32_16x16x32_bf16 v[10:13], v[174:177], v[198:201], v[10:13]
	v_mfma_f32_16x16x32_bf16 v[6:9], v[166:169], v[206:209], v[6:9]
	v_mfma_f32_16x16x32_bf16 v[2:5], v[174:177], v[206:209], v[2:5]
	v_mfma_f32_16x16x32_bf16 v[50:53], v[170:173], v[186:189], v[50:53]
	v_mfma_f32_16x16x32_bf16 v[42:45], v[178:181], v[186:189], v[42:45]
	v_mfma_f32_16x16x32_bf16 v[34:37], v[170:173], v[194:197], v[34:37]
	v_mfma_f32_16x16x32_bf16 v[26:29], v[178:181], v[194:197], v[26:29]
	v_mfma_f32_16x16x32_bf16 v[18:21], v[170:173], v[202:205], v[18:21]
	v_mfma_f32_16x16x32_bf16 v[10:13], v[178:181], v[202:205], v[10:13]
	v_mfma_f32_16x16x32_bf16 v[6:9], v[170:173], v[210:213], v[6:9]
	v_mfma_f32_16x16x32_bf16 v[2:5], v[178:181], v[210:213], v[2:5]
	s_barrier
	s_add_i32 s80, s80, 2
	s_add_u32 s74, s74, 0x10000
	s_addc_u32 s75, s75, 0
	s_add_u32 s58, s58, 0x100
	s_addc_u32 s59, s59, 0
	s_cmp_gt_u32 s80, 29
	s_cbranch_scc0 .LBB0_1271
	s_and_b64 vcc, exec, s[24:25]
	s_cbranch_vccz .LBB0_1274
	s_barrier
	s_setprio 3

.LBB0_1487:
	s_setprio 0
	s_andn2_b64 vcc, exec, s[0:1]
	s_mov_b32 s52, s46
	s_mov_b32 s54, s48
	v_mov_b64_e32 v[2:3], v[174:175]
	s_mov_b64 s[56:57], s[50:51]
	s_cbranch_vccz .LBB0_1503

.LBB0_1497:
	ds_read_b128 v[26:29], v186
	ds_read_b128 v[30:33], v186 offset:1024
	ds_read_b128 v[18:21], v186 offset:2048
	ds_read_b128 v[22:25], v186 offset:3072
	ds_read_b128 v[10:13], v187
	ds_read_b128 v[14:17], v187 offset:1024
	ds_read_b128 v[2:5], v187 offset:2048
	ds_read_b128 v[6:9], v187 offset:3072
	s_add_u32 s56, s4, 0xfffc0080
	s_addc_u32 s57, s5, -1
	s_cmp_eq_u32 s49, 12
	s_cselect_b64 vcc, -1, 0
	s_cselect_b32 s57, s2, s57
	s_cselect_b32 s56, s47, s56
	v_cndmask_b32_e32 v179, v177, v175, vcc
	v_cndmask_b32_e32 v178, v176, v174, vcc
	v_lshl_add_u64 v[180:181], s[4:5], 0, v[168:169]
	s_add_i32 m0, s62, 0xc000
	ds_read_b128 v[192:195], v188
	ds_read_b128 v[196:199], v188 offset:1024
	ds_read_b128 v[200:203], v188 offset:2048
	ds_read_b128 v[204:207], v188 offset:3072
	ds_read_b128 v[208:211], v188 offset:4096
	ds_read_b128 v[212:215], v188 offset:5120
	ds_read_b128 v[220:223], v188 offset:6144
	ds_read_b128 v[224:227], v188 offset:7168
	global_load_lds_dwordx4 v[180:181], off
	v_lshl_add_u64 v[180:181], s[4:5], 0, v[170:171]
	s_add_i32 m0, s62, 0xe000
	s_nop 0
	global_load_lds_dwordx4 v[180:181], off
	s_waitcnt vmcnt(8)
	s_waitcnt lgkmcnt(0)
	s_barrier
	v_mfma_scale_f32_16x16x128_f8f6f4 v[158:161], v[26:33], v[192:199], v[158:161], v189, v190 op_sel_hi:[0,0,0]
	v_mfma_scale_f32_16x16x128_f8f6f4 v[150:153], v[18:25], v[192:199], v[150:153], v189, v190 op_sel_hi:[0,0,0]
	v_mfma_scale_f32_16x16x128_f8f6f4 v[142:145], v[26:33], v[200:207], v[142:145], v189, v190 op_sel_hi:[0,0,0]
	v_mfma_scale_f32_16x16x128_f8f6f4 v[134:137], v[18:25], v[200:207], v[134:137], v189, v190 op_sel_hi:[0,0,0]
	v_mfma_scale_f32_16x16x128_f8f6f4 v[126:129], v[26:33], v[208:215], v[126:129], v189, v190 op_sel_hi:[0,0,0]
	v_mfma_scale_f32_16x16x128_f8f6f4 v[118:121], v[18:25], v[208:215], v[118:121], v189, v190 op_sel_hi:[0,0,0]
	v_mfma_scale_f32_16x16x128_f8f6f4 v[110:113], v[26:33], v[220:227], v[110:113], v189, v190 op_sel_hi:[0,0,0]
	v_mfma_scale_f32_16x16x128_f8f6f4 v[102:105], v[18:25], v[220:227], v[102:105], v189, v190 op_sel_hi:[0,0,0]
	v_mfma_scale_f32_16x16x128_f8f6f4 v[154:157], v[10:17], v[192:199], v[154:157], v189, v190 op_sel_hi:[0,0,0]
	v_mfma_scale_f32_16x16x128_f8f6f4 v[146:149], v[2:9], v[192:199], v[146:149], v189, v190 op_sel_hi:[0,0,0]
	v_mfma_scale_f32_16x16x128_f8f6f4 v[138:141], v[10:17], v[200:207], v[138:141], v189, v190 op_sel_hi:[0,0,0]
	v_mfma_scale_f32_16x16x128_f8f6f4 v[130:133], v[2:9], v[200:207], v[130:133], v189, v190 op_sel_hi:[0,0,0]
	v_mfma_scale_f32_16x16x128_f8f6f4 v[122:125], v[10:17], v[208:215], v[122:125], v189, v190 op_sel_hi:[0,0,0]
	v_mfma_scale_f32_16x16x128_f8f6f4 v[114:117], v[2:9], v[208:215], v[114:117], v189, v190 op_sel_hi:[0,0,0]
	v_mfma_scale_f32_16x16x128_f8f6f4 v[106:109], v[10:17], v[220:227], v[106:109], v189, v190 op_sel_hi:[0,0,0]
	v_mfma_scale_f32_16x16x128_f8f6f4 v[98:101], v[2:9], v[220:227], v[98:101], v189, v190 op_sel_hi:[0,0,0]
	s_barrier
	s_add_i32 s73, s69, s61
	v_lshl_add_u64 v[178:179], v[178:179], 0, v[162:163]
	s_mov_b32 m0, s73
	ds_read_b128 v[192:195], v188 offset:16384
	ds_read_b128 v[196:199], v188 offset:17408
	ds_read_b128 v[200:203], v188 offset:18432
	ds_read_b128 v[204:207], v188 offset:19456
	ds_read_b128 v[208:211], v188 offset:20480
	ds_read_b128 v[212:215], v188 offset:21504
	ds_read_b128 v[220:223], v188 offset:22528
	ds_read_b128 v[224:227], v188 offset:23552
	global_load_lds_dwordx4 v[178:179], off
	v_lshl_add_u64 v[180:181], v[178:179], 0, s[10:11]
	s_add_i32 m0, s73, 0x2000
	s_add_i32 s73, s70, s61
	global_load_lds_dwordx4 v[180:181], off
	v_lshl_add_u64 v[180:181], v[178:179], 0, s[12:13]
	s_mov_b32 m0, s73
	v_lshl_add_u64 v[182:183], s[56:57], 0, v[166:167]
	global_load_lds_dwordx4 v[180:181], off
	v_lshl_add_u64 v[180:181], v[178:179], 0, s[14:15]
	s_add_i32 m0, s73, 0x2000
	s_nop 0
	global_load_lds_dwordx4 v[180:181], off
	v_lshl_add_u64 v[180:181], s[56:57], 0, v[164:165]
	s_mov_b32 m0, s62
	s_nop 0
	global_load_lds_dwordx4 v[180:181], off
	s_mov_b32 m0, s53
	s_nop 0
	global_load_lds_dwordx4 v[182:183], off
	s_waitcnt vmcnt(8)
	s_waitcnt lgkmcnt(0)
	s_barrier
	v_mfma_scale_f32_16x16x128_f8f6f4 v[94:97], v[26:33], v[192:199], v[94:97], v189, v190 op_sel_hi:[0,0,0]
	v_mfma_scale_f32_16x16x128_f8f6f4 v[86:89], v[18:25], v[192:199], v[86:89], v189, v190 op_sel_hi:[0,0,0]
	v_mfma_scale_f32_16x16x128_f8f6f4 v[78:81], v[26:33], v[200:207], v[78:81], v189, v190 op_sel_hi:[0,0,0]
	v_mfma_scale_f32_16x16x128_f8f6f4 v[70:73], v[18:25], v[200:207], v[70:73], v189, v190 op_sel_hi:[0,0,0]
	v_mfma_scale_f32_16x16x128_f8f6f4 v[62:65], v[26:33], v[208:215], v[62:65], v189, v190 op_sel_hi:[0,0,0]
	v_mfma_scale_f32_16x16x128_f8f6f4 v[54:57], v[18:25], v[208:215], v[54:57], v189, v190 op_sel_hi:[0,0,0]
	v_mfma_scale_f32_16x16x128_f8f6f4 v[46:49], v[26:33], v[220:227], v[46:49], v189, v190 op_sel_hi:[0,0,0]
	v_mfma_scale_f32_16x16x128_f8f6f4 v[38:41], v[18:25], v[220:227], v[38:41], v189, v190 op_sel_hi:[0,0,0]
	v_mfma_scale_f32_16x16x128_f8f6f4 v[90:93], v[10:17], v[192:199], v[90:93], v189, v190 op_sel_hi:[0,0,0]
	v_mfma_scale_f32_16x16x128_f8f6f4 v[82:85], v[2:9], v[192:199], v[82:85], v189, v190 op_sel_hi:[0,0,0]
	v_mfma_scale_f32_16x16x128_f8f6f4 v[74:77], v[10:17], v[200:207], v[74:77], v189, v190 op_sel_hi:[0,0,0]
	v_mfma_scale_f32_16x16x128_f8f6f4 v[66:69], v[2:9], v[200:207], v[66:69], v189, v190 op_sel_hi:[0,0,0]
	v_mfma_scale_f32_16x16x128_f8f6f4 v[58:61], v[10:17], v[208:215], v[58:61], v189, v190 op_sel_hi:[0,0,0]
	v_mfma_scale_f32_16x16x128_f8f6f4 v[50:53], v[2:9], v[208:215], v[50:53], v189, v190 op_sel_hi:[0,0,0]
	v_mfma_scale_f32_16x16x128_f8f6f4 v[42:45], v[10:17], v[220:227], v[42:45], v189, v190 op_sel_hi:[0,0,0]
	v_mfma_scale_f32_16x16x128_f8f6f4 v[34:37], v[2:9], v[220:227], v[34:37], v189, v190 op_sel_hi:[0,0,0]
	s_barrier
	s_add_i32 s73, 0, 0x18000
	s_add_i32 s74, 0, 0x1c000
	v_add_u32_e32 v14, s73, v184
	v_add_u32_e32 v30, s74, v184
	ds_read_b128 v[2:5], v14
	ds_read_b128 v[6:9], v14 offset:1024
	ds_read_b128 v[10:13], v14 offset:2048
	ds_read_b128 v[14:17], v14 offset:3072
	ds_read_b128 v[18:21], v30
	ds_read_b128 v[22:25], v30 offset:1024
	ds_read_b128 v[26:29], v30 offset:2048
	ds_read_b128 v[30:33], v30 offset:3072
	s_add_u32 s56, s56, 0x40000
	s_addc_u32 s57, s57, 0
	s_mov_b32 m0, s63
	v_lshl_add_u64 v[216:217], s[56:57], 0, v[164:165]
	ds_read_b128 v[192:195], v188 offset:32768
	ds_read_b128 v[196:199], v188 offset:33792
	ds_read_b128 v[200:203], v188 offset:34816
	ds_read_b128 v[204:207], v188 offset:35840
	ds_read_b128 v[208:211], v188 offset:36864
	ds_read_b128 v[212:215], v188 offset:37888
	ds_read_b128 v[220:223], v188 offset:38912
	ds_read_b128 v[224:227], v188 offset:39936
	global_load_lds_dwordx4 v[216:217], off
	v_lshl_add_u64 v[216:217], s[56:57], 0, v[166:167]
	s_mov_b32 m0, s64
	s_nop 0
	global_load_lds_dwordx4 v[216:217], off
	s_waitcnt vmcnt(8)
	s_waitcnt lgkmcnt(0)
	s_barrier
	v_mfma_scale_f32_16x16x128_f8f6f4 v[158:161], v[2:9], v[192:199], v[158:161], v189, v190 op_sel_hi:[0,0,0]
	v_mfma_scale_f32_16x16x128_f8f6f4 v[150:153], v[10:17], v[192:199], v[150:153], v189, v190 op_sel_hi:[0,0,0]
	v_mfma_scale_f32_16x16x128_f8f6f4 v[142:145], v[2:9], v[200:207], v[142:145], v189, v190 op_sel_hi:[0,0,0]
	v_mfma_scale_f32_16x16x128_f8f6f4 v[134:137], v[10:17], v[200:207], v[134:137], v189, v190 op_sel_hi:[0,0,0]
	v_mfma_scale_f32_16x16x128_f8f6f4 v[126:129], v[2:9], v[208:215], v[126:129], v189, v190 op_sel_hi:[0,0,0]
	v_mfma_scale_f32_16x16x128_f8f6f4 v[118:121], v[10:17], v[208:215], v[118:121], v189, v190 op_sel_hi:[0,0,0]
	v_mfma_scale_f32_16x16x128_f8f6f4 v[110:113], v[2:9], v[220:227], v[110:113], v189, v190 op_sel_hi:[0,0,0]
	v_mfma_scale_f32_16x16x128_f8f6f4 v[102:105], v[10:17], v[220:227], v[102:105], v189, v190 op_sel_hi:[0,0,0]
	v_mfma_scale_f32_16x16x128_f8f6f4 v[154:157], v[18:25], v[192:199], v[154:157], v189, v190 op_sel_hi:[0,0,0]
	v_mfma_scale_f32_16x16x128_f8f6f4 v[146:149], v[26:33], v[192:199], v[146:149], v189, v190 op_sel_hi:[0,0,0]
	v_mfma_scale_f32_16x16x128_f8f6f4 v[138:141], v[18:25], v[200:207], v[138:141], v189, v190 op_sel_hi:[0,0,0]
	v_mfma_scale_f32_16x16x128_f8f6f4 v[130:133], v[26:33], v[200:207], v[130:133], v189, v190 op_sel_hi:[0,0,0]
	v_mfma_scale_f32_16x16x128_f8f6f4 v[122:125], v[18:25], v[208:215], v[122:125], v189, v190 op_sel_hi:[0,0,0]
	v_mfma_scale_f32_16x16x128_f8f6f4 v[114:117], v[26:33], v[208:215], v[114:117], v189, v190 op_sel_hi:[0,0,0]
	v_mfma_scale_f32_16x16x128_f8f6f4 v[106:109], v[18:25], v[220:227], v[106:109], v189, v190 op_sel_hi:[0,0,0]
	v_mfma_scale_f32_16x16x128_f8f6f4 v[98:101], v[26:33], v[220:227], v[98:101], v189, v190 op_sel_hi:[0,0,0]
	s_barrier
	s_add_i32 s56, s73, s61
	v_lshl_add_u64 v[216:217], v[178:179], 0, s[20:21]
	s_mov_b32 m0, s56
	ds_read_b128 v[192:195], v188 offset:49152
	ds_read_b128 v[196:199], v188 offset:50176
	ds_read_b128 v[200:203], v188 offset:51200
	ds_read_b128 v[204:207], v188 offset:52224
	ds_read_b128 v[208:211], v188 offset:53248
	ds_read_b128 v[212:215], v188 offset:54272
	ds_read_b128 v[220:223], v188 offset:55296
	ds_read_b128 v[224:227], v188 offset:56320
	global_load_lds_dwordx4 v[216:217], off
	v_lshl_add_u64 v[216:217], v[178:179], 0, s[22:23]
	s_add_i32 m0, s56, 0x2000
	s_add_i32 s56, s74, s61
	global_load_lds_dwordx4 v[216:217], off
	v_lshl_add_u64 v[216:217], v[178:179], 0, s[26:27]
	s_mov_b32 m0, s56
	v_lshl_add_u64 v[178:179], v[178:179], 0, s[36:37]
	global_load_lds_dwordx4 v[216:217], off
	s_add_i32 m0, s56, 0x2000
	s_nop 0
	global_load_lds_dwordx4 v[178:179], off
	v_lshl_add_u64 v[178:179], v[180:181], 0, s[24:25]
	s_mov_b32 m0, s66
	s_nop 0
	global_load_lds_dwordx4 v[178:179], off
	v_lshl_add_u64 v[178:179], v[182:183], 0, s[24:25]
	s_mov_b32 m0, s67
	s_nop 0
	global_load_lds_dwordx4 v[178:179], off
	s_waitcnt vmcnt(8)
	s_waitcnt lgkmcnt(0)
	s_barrier
	v_mfma_scale_f32_16x16x128_f8f6f4 v[94:97], v[2:9], v[192:199], v[94:97], v189, v190 op_sel_hi:[0,0,0]
	v_mfma_scale_f32_16x16x128_f8f6f4 v[86:89], v[10:17], v[192:199], v[86:89], v189, v190 op_sel_hi:[0,0,0]
	v_mfma_scale_f32_16x16x128_f8f6f4 v[78:81], v[2:9], v[200:207], v[78:81], v189, v190 op_sel_hi:[0,0,0]
	v_mfma_scale_f32_16x16x128_f8f6f4 v[70:73], v[10:17], v[200:207], v[70:73], v189, v190 op_sel_hi:[0,0,0]
	v_mfma_scale_f32_16x16x128_f8f6f4 v[62:65], v[2:9], v[208:215], v[62:65], v189, v190 op_sel_hi:[0,0,0]
	v_mfma_scale_f32_16x16x128_f8f6f4 v[54:57], v[10:17], v[208:215], v[54:57], v189, v190 op_sel_hi:[0,0,0]
	v_mfma_scale_f32_16x16x128_f8f6f4 v[46:49], v[2:9], v[220:227], v[46:49], v189, v190 op_sel_hi:[0,0,0]
	v_mfma_scale_f32_16x16x128_f8f6f4 v[38:41], v[10:17], v[220:227], v[38:41], v189, v190 op_sel_hi:[0,0,0]
	v_mfma_scale_f32_16x16x128_f8f6f4 v[90:93], v[18:25], v[192:199], v[90:93], v189, v190 op_sel_hi:[0,0,0]
	v_mfma_scale_f32_16x16x128_f8f6f4 v[82:85], v[26:33], v[192:199], v[82:85], v189, v190 op_sel_hi:[0,0,0]
	v_mfma_scale_f32_16x16x128_f8f6f4 v[74:77], v[18:25], v[200:207], v[74:77], v189, v190 op_sel_hi:[0,0,0]
	v_mfma_scale_f32_16x16x128_f8f6f4 v[66:69], v[26:33], v[200:207], v[66:69], v189, v190 op_sel_hi:[0,0,0]
	v_mfma_scale_f32_16x16x128_f8f6f4 v[58:61], v[18:25], v[208:215], v[58:61], v189, v190 op_sel_hi:[0,0,0]
	v_mfma_scale_f32_16x16x128_f8f6f4 v[50:53], v[26:33], v[208:215], v[50:53], v189, v190 op_sel_hi:[0,0,0]
	v_mfma_scale_f32_16x16x128_f8f6f4 v[42:45], v[18:25], v[220:227], v[42:45], v189, v190 op_sel_hi:[0,0,0]
	v_mfma_scale_f32_16x16x128_f8f6f4 v[34:37], v[26:33], v[220:227], v[34:37], v189, v190 op_sel_hi:[0,0,0]
	s_barrier
	s_add_i32 s49, s49, 2
	s_add_u32 s4, s4, 0x100
	s_addc_u32 s5, s5, 0
	s_cmp_gt_u32 s49, 13
	v_lshl_add_u64 v[176:177], v[176:177], 0, s[40:41]
	s_cbranch_scc0 .LBB0_1497
	s_and_b64 vcc, exec, s[38:39]
	s_cbranch_vccz .LBB0_1500
	s_barrier
	s_setprio 3

.LBB0_1560:
	s_setprio 0
	s_andn2_b64 vcc, exec, s[0:1]
	s_mov_b32 s2, s75
	s_mov_b32 s54, s52
	v_mov_b64_e32 v[2:3], v[174:175]
	s_mov_b64 s[56:57], s[4:5]
	s_cbranch_vccz .LBB0_1574

.LBB0_1568:
	ds_read_b128 v[26:29], v186
	ds_read_b128 v[30:33], v186 offset:1024
	ds_read_b128 v[18:21], v186 offset:2048
	ds_read_b128 v[22:25], v186 offset:3072
	ds_read_b128 v[10:13], v187
	ds_read_b128 v[14:17], v187 offset:1024
	ds_read_b128 v[2:5], v187 offset:2048
	ds_read_b128 v[6:9], v187 offset:3072
	s_add_u32 s58, s56, 0xfff50080
	s_addc_u32 s59, s57, -1
	s_cmp_eq_u32 s53, 40
	s_cselect_b64 vcc, -1, 0
	s_cselect_b32 s59, s5, s59
	s_cselect_b32 s58, s4, s58
	v_cndmask_b32_e32 v179, v177, v175, vcc
	v_cndmask_b32_e32 v178, v176, v174, vcc
	v_lshl_add_u64 v[180:181], s[56:57], 0, v[170:171]
	s_add_i32 m0, s61, 0xc000
	ds_read_b128 v[192:195], v188
	ds_read_b128 v[196:199], v188 offset:1024
	ds_read_b128 v[200:203], v188 offset:2048
	ds_read_b128 v[204:207], v188 offset:3072
	ds_read_b128 v[208:211], v188 offset:4096
	ds_read_b128 v[212:215], v188 offset:5120
	ds_read_b128 v[220:223], v188 offset:6144
	ds_read_b128 v[224:227], v188 offset:7168
	global_load_lds_dwordx4 v[180:181], off
	v_lshl_add_u64 v[180:181], s[56:57], 0, v[172:173]
	s_add_i32 m0, s61, 0xe000
	s_nop 0
	global_load_lds_dwordx4 v[180:181], off
	s_waitcnt vmcnt(8)
	s_waitcnt lgkmcnt(0)
	s_barrier
	v_mfma_scale_f32_16x16x128_f8f6f4 v[158:161], v[26:33], v[192:199], v[158:161], v189, v190 op_sel_hi:[0,0,0]
	v_mfma_scale_f32_16x16x128_f8f6f4 v[154:157], v[18:25], v[192:199], v[154:157], v189, v190 op_sel_hi:[0,0,0]
	v_mfma_scale_f32_16x16x128_f8f6f4 v[150:153], v[26:33], v[200:207], v[150:153], v189, v190 op_sel_hi:[0,0,0]
	v_mfma_scale_f32_16x16x128_f8f6f4 v[142:145], v[18:25], v[200:207], v[142:145], v189, v190 op_sel_hi:[0,0,0]
	v_mfma_scale_f32_16x16x128_f8f6f4 v[134:137], v[26:33], v[208:215], v[134:137], v189, v190 op_sel_hi:[0,0,0]
	v_mfma_scale_f32_16x16x128_f8f6f4 v[126:129], v[18:25], v[208:215], v[126:129], v189, v190 op_sel_hi:[0,0,0]
	v_mfma_scale_f32_16x16x128_f8f6f4 v[118:121], v[26:33], v[220:227], v[118:121], v189, v190 op_sel_hi:[0,0,0]
	v_mfma_scale_f32_16x16x128_f8f6f4 v[110:113], v[18:25], v[220:227], v[110:113], v189, v190 op_sel_hi:[0,0,0]
	v_mfma_scale_f32_16x16x128_f8f6f4 v[146:149], v[10:17], v[192:199], v[146:149], v189, v190 op_sel_hi:[0,0,0]
	v_mfma_scale_f32_16x16x128_f8f6f4 v[138:141], v[2:9], v[192:199], v[138:141], v189, v190 op_sel_hi:[0,0,0]
	v_mfma_scale_f32_16x16x128_f8f6f4 v[130:133], v[10:17], v[200:207], v[130:133], v189, v190 op_sel_hi:[0,0,0]
	v_mfma_scale_f32_16x16x128_f8f6f4 v[122:125], v[2:9], v[200:207], v[122:125], v189, v190 op_sel_hi:[0,0,0]
	v_mfma_scale_f32_16x16x128_f8f6f4 v[114:117], v[10:17], v[208:215], v[114:117], v189, v190 op_sel_hi:[0,0,0]
	v_mfma_scale_f32_16x16x128_f8f6f4 v[106:109], v[2:9], v[208:215], v[106:109], v189, v190 op_sel_hi:[0,0,0]
	v_mfma_scale_f32_16x16x128_f8f6f4 v[102:105], v[10:17], v[220:227], v[102:105], v189, v190 op_sel_hi:[0,0,0]
	v_mfma_scale_f32_16x16x128_f8f6f4 v[98:101], v[2:9], v[220:227], v[98:101], v189, v190 op_sel_hi:[0,0,0]
	s_barrier
	s_add_i32 s80, s69, s33
	v_lshl_add_u64 v[178:179], v[178:179], 0, v[164:165]
	s_mov_b32 m0, s80
	ds_read_b128 v[192:195], v188 offset:16384
	ds_read_b128 v[196:199], v188 offset:17408
	ds_read_b128 v[200:203], v188 offset:18432
	ds_read_b128 v[204:207], v188 offset:19456
	ds_read_b128 v[208:211], v188 offset:20480
	ds_read_b128 v[212:215], v188 offset:21504
	ds_read_b128 v[220:223], v188 offset:22528
	ds_read_b128 v[224:227], v188 offset:23552
	global_load_lds_dwordx4 v[178:179], off
	v_lshl_add_u64 v[180:181], v[178:179], 0, s[10:11]
	s_add_i32 m0, s80, 0x2000
	s_add_i32 s80, s70, s33
	global_load_lds_dwordx4 v[180:181], off
	v_lshl_add_u64 v[180:181], v[178:179], 0, s[12:13]
	s_mov_b32 m0, s80
	v_lshl_add_u64 v[182:183], s[58:59], 0, v[168:169]
	global_load_lds_dwordx4 v[180:181], off
	v_lshl_add_u64 v[180:181], v[178:179], 0, s[14:15]
	s_add_i32 m0, s80, 0x2000
	s_nop 0
	global_load_lds_dwordx4 v[180:181], off
	v_lshl_add_u64 v[180:181], s[58:59], 0, v[166:167]
	s_mov_b32 m0, s61
	s_nop 0
	global_load_lds_dwordx4 v[180:181], off
	s_mov_b32 m0, s62
	s_nop 0
	global_load_lds_dwordx4 v[182:183], off
	s_waitcnt vmcnt(8)
	s_waitcnt lgkmcnt(0)
	s_barrier
	v_mfma_scale_f32_16x16x128_f8f6f4 v[94:97], v[26:33], v[192:199], v[94:97], v189, v190 op_sel_hi:[0,0,0]
	v_mfma_scale_f32_16x16x128_f8f6f4 v[90:93], v[18:25], v[192:199], v[90:93], v189, v190 op_sel_hi:[0,0,0]
	v_mfma_scale_f32_16x16x128_f8f6f4 v[86:89], v[26:33], v[200:207], v[86:89], v189, v190 op_sel_hi:[0,0,0]
	v_mfma_scale_f32_16x16x128_f8f6f4 v[78:81], v[18:25], v[200:207], v[78:81], v189, v190 op_sel_hi:[0,0,0]
	v_mfma_scale_f32_16x16x128_f8f6f4 v[70:73], v[26:33], v[208:215], v[70:73], v189, v190 op_sel_hi:[0,0,0]
	v_mfma_scale_f32_16x16x128_f8f6f4 v[62:65], v[18:25], v[208:215], v[62:65], v189, v190 op_sel_hi:[0,0,0]
	v_mfma_scale_f32_16x16x128_f8f6f4 v[54:57], v[26:33], v[220:227], v[54:57], v189, v190 op_sel_hi:[0,0,0]
	v_mfma_scale_f32_16x16x128_f8f6f4 v[46:49], v[18:25], v[220:227], v[46:49], v189, v190 op_sel_hi:[0,0,0]
	v_mfma_scale_f32_16x16x128_f8f6f4 v[82:85], v[10:17], v[192:199], v[82:85], v189, v190 op_sel_hi:[0,0,0]
	v_mfma_scale_f32_16x16x128_f8f6f4 v[74:77], v[2:9], v[192:199], v[74:77], v189, v190 op_sel_hi:[0,0,0]
	v_mfma_scale_f32_16x16x128_f8f6f4 v[66:69], v[10:17], v[200:207], v[66:69], v189, v190 op_sel_hi:[0,0,0]
	v_mfma_scale_f32_16x16x128_f8f6f4 v[58:61], v[2:9], v[200:207], v[58:61], v189, v190 op_sel_hi:[0,0,0]
	v_mfma_scale_f32_16x16x128_f8f6f4 v[50:53], v[10:17], v[208:215], v[50:53], v189, v190 op_sel_hi:[0,0,0]
	v_mfma_scale_f32_16x16x128_f8f6f4 v[42:45], v[2:9], v[208:215], v[42:45], v189, v190 op_sel_hi:[0,0,0]
	v_mfma_scale_f32_16x16x128_f8f6f4 v[38:41], v[10:17], v[220:227], v[38:41], v189, v190 op_sel_hi:[0,0,0]
	v_mfma_scale_f32_16x16x128_f8f6f4 v[34:37], v[2:9], v[220:227], v[34:37], v189, v190 op_sel_hi:[0,0,0]
	s_barrier
	s_add_i32 s80, 0, 0x18000
	s_add_i32 s81, 0, 0x1c000
	v_add_u32_e32 v14, s80, v184
	v_add_u32_e32 v30, s81, v184
	ds_read_b128 v[2:5], v14
	ds_read_b128 v[6:9], v14 offset:1024
	ds_read_b128 v[10:13], v14 offset:2048
	ds_read_b128 v[14:17], v14 offset:3072
	ds_read_b128 v[18:21], v30
	ds_read_b128 v[22:25], v30 offset:1024
	ds_read_b128 v[26:29], v30 offset:2048
	ds_read_b128 v[30:33], v30 offset:3072
	s_add_u32 s58, s58, 0xb0000
	s_addc_u32 s59, s59, 0
	s_mov_b32 m0, s63
	v_lshl_add_u64 v[216:217], s[58:59], 0, v[166:167]
	ds_read_b128 v[192:195], v188 offset:32768
	ds_read_b128 v[196:199], v188 offset:33792
	ds_read_b128 v[200:203], v188 offset:34816
	ds_read_b128 v[204:207], v188 offset:35840
	ds_read_b128 v[208:211], v188 offset:36864
	ds_read_b128 v[212:215], v188 offset:37888
	ds_read_b128 v[220:223], v188 offset:38912
	ds_read_b128 v[224:227], v188 offset:39936
	global_load_lds_dwordx4 v[216:217], off
	v_lshl_add_u64 v[216:217], s[58:59], 0, v[168:169]
	s_mov_b32 m0, s64
	s_nop 0
	global_load_lds_dwordx4 v[216:217], off
	s_waitcnt vmcnt(8)
	s_waitcnt lgkmcnt(0)
	s_barrier
	v_mfma_scale_f32_16x16x128_f8f6f4 v[158:161], v[2:9], v[192:199], v[158:161], v189, v190 op_sel_hi:[0,0,0]
	v_mfma_scale_f32_16x16x128_f8f6f4 v[154:157], v[10:17], v[192:199], v[154:157], v189, v190 op_sel_hi:[0,0,0]
	v_mfma_scale_f32_16x16x128_f8f6f4 v[150:153], v[2:9], v[200:207], v[150:153], v189, v190 op_sel_hi:[0,0,0]
	v_mfma_scale_f32_16x16x128_f8f6f4 v[142:145], v[10:17], v[200:207], v[142:145], v189, v190 op_sel_hi:[0,0,0]
	v_mfma_scale_f32_16x16x128_f8f6f4 v[134:137], v[2:9], v[208:215], v[134:137], v189, v190 op_sel_hi:[0,0,0]
	v_mfma_scale_f32_16x16x128_f8f6f4 v[126:129], v[10:17], v[208:215], v[126:129], v189, v190 op_sel_hi:[0,0,0]
	v_mfma_scale_f32_16x16x128_f8f6f4 v[118:121], v[2:9], v[220:227], v[118:121], v189, v190 op_sel_hi:[0,0,0]
	v_mfma_scale_f32_16x16x128_f8f6f4 v[110:113], v[10:17], v[220:227], v[110:113], v189, v190 op_sel_hi:[0,0,0]
	v_mfma_scale_f32_16x16x128_f8f6f4 v[146:149], v[18:25], v[192:199], v[146:149], v189, v190 op_sel_hi:[0,0,0]
	v_mfma_scale_f32_16x16x128_f8f6f4 v[138:141], v[26:33], v[192:199], v[138:141], v189, v190 op_sel_hi:[0,0,0]
	v_mfma_scale_f32_16x16x128_f8f6f4 v[130:133], v[18:25], v[200:207], v[130:133], v189, v190 op_sel_hi:[0,0,0]
	v_mfma_scale_f32_16x16x128_f8f6f4 v[122:125], v[26:33], v[200:207], v[122:125], v189, v190 op_sel_hi:[0,0,0]
	v_mfma_scale_f32_16x16x128_f8f6f4 v[114:117], v[18:25], v[208:215], v[114:117], v189, v190 op_sel_hi:[0,0,0]
	v_mfma_scale_f32_16x16x128_f8f6f4 v[106:109], v[26:33], v[208:215], v[106:109], v189, v190 op_sel_hi:[0,0,0]
	v_mfma_scale_f32_16x16x128_f8f6f4 v[102:105], v[18:25], v[220:227], v[102:105], v189, v190 op_sel_hi:[0,0,0]
	v_mfma_scale_f32_16x16x128_f8f6f4 v[98:101], v[26:33], v[220:227], v[98:101], v189, v190 op_sel_hi:[0,0,0]
	s_barrier
	s_add_i32 s58, s80, s33
	v_lshl_add_u64 v[216:217], v[178:179], 0, s[24:25]
	s_mov_b32 m0, s58
	ds_read_b128 v[192:195], v188 offset:49152
	ds_read_b128 v[196:199], v188 offset:50176
	ds_read_b128 v[200:203], v188 offset:51200
	ds_read_b128 v[204:207], v188 offset:52224
	ds_read_b128 v[208:211], v188 offset:53248
	ds_read_b128 v[212:215], v188 offset:54272
	ds_read_b128 v[220:223], v188 offset:55296
	ds_read_b128 v[224:227], v188 offset:56320
	global_load_lds_dwordx4 v[216:217], off
	v_lshl_add_u64 v[216:217], v[178:179], 0, s[26:27]
	s_add_i32 m0, s58, 0x2000
	s_add_i32 s58, s81, s33
	global_load_lds_dwordx4 v[216:217], off
	v_lshl_add_u64 v[216:217], v[178:179], 0, s[38:39]
	s_mov_b32 m0, s58
	v_lshl_add_u64 v[178:179], v[178:179], 0, s[40:41]
	global_load_lds_dwordx4 v[216:217], off
	s_add_i32 m0, s58, 0x2000
	s_nop 0
	global_load_lds_dwordx4 v[178:179], off
	v_lshl_add_u64 v[178:179], v[180:181], 0, s[36:37]
	s_mov_b32 m0, s66
	s_nop 0
	global_load_lds_dwordx4 v[178:179], off
	v_lshl_add_u64 v[178:179], v[182:183], 0, s[36:37]
	s_mov_b32 m0, s67
	s_nop 0
	global_load_lds_dwordx4 v[178:179], off
	s_waitcnt vmcnt(8)
	s_waitcnt lgkmcnt(0)
	s_barrier
	v_mfma_scale_f32_16x16x128_f8f6f4 v[94:97], v[2:9], v[192:199], v[94:97], v189, v190 op_sel_hi:[0,0,0]
	v_mfma_scale_f32_16x16x128_f8f6f4 v[90:93], v[10:17], v[192:199], v[90:93], v189, v190 op_sel_hi:[0,0,0]
	v_mfma_scale_f32_16x16x128_f8f6f4 v[86:89], v[2:9], v[200:207], v[86:89], v189, v190 op_sel_hi:[0,0,0]
	v_mfma_scale_f32_16x16x128_f8f6f4 v[78:81], v[10:17], v[200:207], v[78:81], v189, v190 op_sel_hi:[0,0,0]
	v_mfma_scale_f32_16x16x128_f8f6f4 v[70:73], v[2:9], v[208:215], v[70:73], v189, v190 op_sel_hi:[0,0,0]
	v_mfma_scale_f32_16x16x128_f8f6f4 v[62:65], v[10:17], v[208:215], v[62:65], v189, v190 op_sel_hi:[0,0,0]
	v_mfma_scale_f32_16x16x128_f8f6f4 v[54:57], v[2:9], v[220:227], v[54:57], v189, v190 op_sel_hi:[0,0,0]
	v_mfma_scale_f32_16x16x128_f8f6f4 v[46:49], v[10:17], v[220:227], v[46:49], v189, v190 op_sel_hi:[0,0,0]
	v_mfma_scale_f32_16x16x128_f8f6f4 v[82:85], v[18:25], v[192:199], v[82:85], v189, v190 op_sel_hi:[0,0,0]
	v_mfma_scale_f32_16x16x128_f8f6f4 v[74:77], v[26:33], v[192:199], v[74:77], v189, v190 op_sel_hi:[0,0,0]
	v_mfma_scale_f32_16x16x128_f8f6f4 v[66:69], v[18:25], v[200:207], v[66:69], v189, v190 op_sel_hi:[0,0,0]
	v_mfma_scale_f32_16x16x128_f8f6f4 v[58:61], v[26:33], v[200:207], v[58:61], v189, v190 op_sel_hi:[0,0,0]
	v_mfma_scale_f32_16x16x128_f8f6f4 v[50:53], v[18:25], v[208:215], v[50:53], v189, v190 op_sel_hi:[0,0,0]
	v_mfma_scale_f32_16x16x128_f8f6f4 v[42:45], v[26:33], v[208:215], v[42:45], v189, v190 op_sel_hi:[0,0,0]
	v_mfma_scale_f32_16x16x128_f8f6f4 v[38:41], v[18:25], v[220:227], v[38:41], v189, v190 op_sel_hi:[0,0,0]
	v_mfma_scale_f32_16x16x128_f8f6f4 v[34:37], v[26:33], v[220:227], v[34:37], v189, v190 op_sel_hi:[0,0,0]
	s_barrier
	s_add_i32 s53, s53, 2
	s_add_u32 s56, s56, 0x100
	s_addc_u32 s57, s57, 0
	s_cmp_gt_u32 s53, 41
	v_lshl_add_u64 v[176:177], v[176:177], 0, s[44:45]
	s_cbranch_scc0 .LBB0_1568
	s_and_b64 vcc, exec, s[42:43]
	s_cbranch_vccz .LBB0_1571
	s_barrier
	s_setprio 3
